# P2: dedicated converter workgroups run a hand-written software-pipelined expert-weight converter (4 items = 32 KB in flight per wave, batches of 32, counted vmcnt); nconv still 72
# baseline (speedup 1.0000x reference)
.LBB0_178:
	s_cmp_lt_i32 s60, 3
	s_cselect_b64 s[8:9], -1, 0
	v_writelane_b32 v252, s60, 57
	s_and_b64 s[2:3], s[8:9], s[2:3]
	s_andn2_b64 vcc, exec, s[2:3]
	v_writelane_b32 v252, s61, 58
	v_writelane_b32 v252, s56, 59
	s_cbranch_vccnz .LBB0_289
	s_cmpk_gt_i32 s62, 0x7f
	s_cselect_b32 s2, 0xffffffb8, 0
	s_add_i32 s33, s2, s62
	s_mov_b32 s7, 0
	s_cmp_lt_i32 s80, s33
	s_mov_b64 s[2:3], -1
	s_cbranch_scc1 .LBB0_208
	s_load_dwordx2 s[10:11], s[0:1], 0x128
	s_load_dwordx4 s[12:15], s[0:1], 0xe8
	s_load_dwordx4 s[16:19], s[0:1], 0xf8
	s_load_dwordx4 s[20:23], s[0:1], 0x108
	v_mov_b32_e32 v1, 0x43e00000
	s_mov_b32 s27, 0xc3e00000
	v_and_b32_e32 v25, 7, v206
	v_lshrrev_b32_e32 v26, 3, v206
	v_lshlrev_b32_e32 v10, 4, v25
	v_lshlrev_b32_e32 v11, 11, v25
	v_lshlrev_b32_e32 v12, 3, v26
	v_lshlrev_b32_e32 v2, 14, v26
	v_add_u32_e32 v3, 2048, v2
	v_add_u32_e32 v4, 4096, v2
	v_add_u32_e32 v5, 6144, v2
	v_add_u32_e32 v6, 8192, v2
	v_add_u32_e32 v7, 10240, v2
	v_add_u32_e32 v8, 12288, v2
	v_add_u32_e32 v9, 14336, v2
	v_mov_b32_e32 v26, 0
	s_waitcnt lgkmcnt(0)
	s_add_u32 s46, s10, 0x14000
	s_addc_u32 s47, s11, 0
.Lcv_batch:
	v_mov_b32_e32 v25, 32
	v_cmp_eq_u32_e32 vcc, 0, v206
	s_and_saveexec_b64 s[2:3], vcc
	global_atomic_add v25, v26, v25, s[46:47] sc0
	s_mov_b64 exec, s[2:3]
	s_waitcnt vmcnt(0)
	v_readfirstlane_b32 s24, v25
	s_cmp_ge_u32 s24, 0x18600
	s_cbranch_scc1 .LBB0_207
	s_sub_u32 s25, 0x18600, s24
	s_min_u32 s25, s25, 32
	s_add_u32 s38, s24, 0
	s_sub_u32 s2, s38, 0x10400
	s_cmp_ge_u32 s38, 0x10400
	s_cselect_b32 s3, s2, s38
	s_cselect_b32 s6, 1, 0
	s_cmp_ge_u32 s3, 0x8200
	s_cselect_b32 s7, 1, 0
	s_mul_i32 s2, s7, 0x8200
	s_sub_u32 s3, s3, s2
	s_lshr_b32 s34, s3, 9
	s_and_b32 s3, s3, 0x1ff
	s_cmp_eq_u32 s6, 1
	s_cselect_b32 s35, 7, 5
	s_cselect_b32 s45, 63, 15
	s_lshr_b32 s2, s3, s35
	s_lshl_b32 s2, s2, 1
	s_and_b32 s39, s3, 1
	s_or_b32 s39, s2, s39
	s_lshr_b32 s2, s3, 1
	s_and_b32 s40, s2, s45
	s_cmp_eq_u32 s7, 1
	s_cselect_b64 s[44:45], s[14:15], s[12:13]
	s_cselect_b64 s[2:3], s[20:21], s[18:19]
	s_cmp_eq_u32 s6, 1
	s_cselect_b64 s[44:45], s[16:17], s[44:45]
	s_cselect_b64 s[2:3], s[22:23], s[2:3]
	s_cselect_b32 s35, 19, 17
	s_cselect_b32 s36, 2, 0
	s_cmp_lt_u32 s34, 64
	s_cselect_b64 s[28:29], s[44:45], s[2:3]
	s_cselect_b32 s34, s34, 0
	s_lshl_b32 s34, s34, 22
	s_lshl_b32 s2, s39, s35
	s_add_u32 s34, s34, s2
	s_lshl_b32 s2, s40, 7
	s_add_u32 s34, s34, s2
	s_add_u32 s28, s28, s34
	s_addc_u32 s29, s29, 0
	v_lshl_add_u32 v13, v2, s36, v10
	v_lshl_add_u32 v14, v3, s36, v10
	v_lshl_add_u32 v15, v4, s36, v10
	v_lshl_add_u32 v16, v5, s36, v10
	v_lshl_add_u32 v17, v6, s36, v10
	v_lshl_add_u32 v18, v7, s36, v10
	v_lshl_add_u32 v19, v8, s36, v10
	v_lshl_add_u32 v20, v9, s36, v10
	global_load_dwordx4 v[48:51], v13, s[28:29]
	global_load_dwordx4 v[52:55], v14, s[28:29]
	global_load_dwordx4 v[56:59], v15, s[28:29]
	global_load_dwordx4 v[60:63], v16, s[28:29]
	global_load_dwordx4 v[64:67], v17, s[28:29]
	global_load_dwordx4 v[68:71], v18, s[28:29]
	global_load_dwordx4 v[72:75], v19, s[28:29]
	global_load_dwordx4 v[76:79], v20, s[28:29]
	s_add_u32 s38, s24, 1
	s_sub_u32 s2, s38, 0x10400
	s_cmp_ge_u32 s38, 0x10400
	s_cselect_b32 s3, s2, s38
	s_cselect_b32 s6, 1, 0
	s_cmp_ge_u32 s3, 0x8200
	s_cselect_b32 s7, 1, 0
	s_mul_i32 s2, s7, 0x8200
	s_sub_u32 s3, s3, s2
	s_lshr_b32 s34, s3, 9
	s_and_b32 s3, s3, 0x1ff
	s_cmp_eq_u32 s6, 1
	s_cselect_b32 s35, 7, 5
	s_cselect_b32 s45, 63, 15
	s_lshr_b32 s2, s3, s35
	s_lshl_b32 s2, s2, 1
	s_and_b32 s39, s3, 1
	s_or_b32 s39, s2, s39
	s_lshr_b32 s2, s3, 1
	s_and_b32 s40, s2, s45
	s_cmp_eq_u32 s7, 1
	s_cselect_b64 s[44:45], s[14:15], s[12:13]
	s_cselect_b64 s[2:3], s[20:21], s[18:19]
	s_cmp_eq_u32 s6, 1
	s_cselect_b64 s[44:45], s[16:17], s[44:45]
	s_cselect_b64 s[2:3], s[22:23], s[2:3]
	s_cselect_b32 s35, 19, 17
	s_cselect_b32 s36, 2, 0
	s_cmp_lt_u32 s34, 64
	s_cselect_b64 s[42:43], s[44:45], s[2:3]
	s_cselect_b32 s34, s34, 0
	s_lshl_b32 s34, s34, 22
	s_lshl_b32 s2, s39, s35
	s_add_u32 s34, s34, s2
	s_lshl_b32 s2, s40, 7
	s_add_u32 s34, s34, s2
	s_add_u32 s42, s42, s34
	s_addc_u32 s43, s43, 0
	v_lshl_add_u32 v13, v2, s36, v10
	v_lshl_add_u32 v14, v3, s36, v10
	v_lshl_add_u32 v15, v4, s36, v10
	v_lshl_add_u32 v16, v5, s36, v10
	v_lshl_add_u32 v17, v6, s36, v10
	v_lshl_add_u32 v18, v7, s36, v10
	v_lshl_add_u32 v19, v8, s36, v10
	v_lshl_add_u32 v20, v9, s36, v10
	global_load_dwordx4 v[80:83], v13, s[42:43]
	global_load_dwordx4 v[84:87], v14, s[42:43]
	global_load_dwordx4 v[88:91], v15, s[42:43]
	global_load_dwordx4 v[92:95], v16, s[42:43]
	global_load_dwordx4 v[96:99], v17, s[42:43]
	global_load_dwordx4 v[100:103], v18, s[42:43]
	global_load_dwordx4 v[104:107], v19, s[42:43]
	global_load_dwordx4 v[108:111], v20, s[42:43]
	s_add_u32 s38, s24, 2
	s_sub_u32 s2, s38, 0x10400
	s_cmp_ge_u32 s38, 0x10400
	s_cselect_b32 s3, s2, s38
	s_cselect_b32 s6, 1, 0
	s_cmp_ge_u32 s3, 0x8200
	s_cselect_b32 s7, 1, 0
	s_mul_i32 s2, s7, 0x8200
	s_sub_u32 s3, s3, s2
	s_lshr_b32 s34, s3, 9
	s_and_b32 s3, s3, 0x1ff
	s_cmp_eq_u32 s6, 1
	s_cselect_b32 s35, 7, 5
	s_cselect_b32 s45, 63, 15
	s_lshr_b32 s2, s3, s35
	s_lshl_b32 s2, s2, 1
	s_and_b32 s39, s3, 1
	s_or_b32 s39, s2, s39
	s_lshr_b32 s2, s3, 1
	s_and_b32 s40, s2, s45
	s_cmp_eq_u32 s7, 1
	s_cselect_b64 s[44:45], s[14:15], s[12:13]
	s_cselect_b64 s[2:3], s[20:21], s[18:19]
	s_cmp_eq_u32 s6, 1
	s_cselect_b64 s[44:45], s[16:17], s[44:45]
	s_cselect_b64 s[2:3], s[22:23], s[2:3]
	s_cselect_b32 s35, 19, 17
	s_cselect_b32 s36, 2, 0
	s_cmp_lt_u32 s34, 64
	s_cselect_b64 s[28:29], s[44:45], s[2:3]
	s_cselect_b32 s34, s34, 0
	s_lshl_b32 s34, s34, 22
	s_lshl_b32 s2, s39, s35
	s_add_u32 s34, s34, s2
	s_lshl_b32 s2, s40, 7
	s_add_u32 s34, s34, s2
	s_add_u32 s28, s28, s34
	s_addc_u32 s29, s29, 0
	v_lshl_add_u32 v13, v2, s36, v10
	v_lshl_add_u32 v14, v3, s36, v10
	v_lshl_add_u32 v15, v4, s36, v10
	v_lshl_add_u32 v16, v5, s36, v10
	v_lshl_add_u32 v17, v6, s36, v10
	v_lshl_add_u32 v18, v7, s36, v10
	v_lshl_add_u32 v19, v8, s36, v10
	v_lshl_add_u32 v20, v9, s36, v10
	global_load_dwordx4 v[112:115], v13, s[28:29]
	global_load_dwordx4 v[116:119], v14, s[28:29]
	global_load_dwordx4 v[120:123], v15, s[28:29]
	global_load_dwordx4 v[124:127], v16, s[28:29]
	global_load_dwordx4 v[128:131], v17, s[28:29]
	global_load_dwordx4 v[132:135], v18, s[28:29]
	global_load_dwordx4 v[136:139], v19, s[28:29]
	global_load_dwordx4 v[140:143], v20, s[28:29]
	s_add_u32 s38, s24, 3
	s_sub_u32 s2, s38, 0x10400
	s_cmp_ge_u32 s38, 0x10400
	s_cselect_b32 s3, s2, s38
	s_cselect_b32 s6, 1, 0
	s_cmp_ge_u32 s3, 0x8200
	s_cselect_b32 s7, 1, 0
	s_mul_i32 s2, s7, 0x8200
	s_sub_u32 s3, s3, s2
	s_lshr_b32 s34, s3, 9
	s_and_b32 s3, s3, 0x1ff
	s_cmp_eq_u32 s6, 1
	s_cselect_b32 s35, 7, 5
	s_cselect_b32 s45, 63, 15
	s_lshr_b32 s2, s3, s35
	s_lshl_b32 s2, s2, 1
	s_and_b32 s39, s3, 1
	s_or_b32 s39, s2, s39
	s_lshr_b32 s2, s3, 1
	s_and_b32 s40, s2, s45
	s_cmp_eq_u32 s7, 1
	s_cselect_b64 s[44:45], s[14:15], s[12:13]
	s_cselect_b64 s[2:3], s[20:21], s[18:19]
	s_cmp_eq_u32 s6, 1
	s_cselect_b64 s[44:45], s[16:17], s[44:45]
	s_cselect_b64 s[2:3], s[22:23], s[2:3]
	s_cselect_b32 s35, 19, 17
	s_cselect_b32 s36, 2, 0
	s_cmp_lt_u32 s34, 64
	s_cselect_b64 s[42:43], s[44:45], s[2:3]
	s_cselect_b32 s34, s34, 0
	s_lshl_b32 s34, s34, 22
	s_lshl_b32 s2, s39, s35
	s_add_u32 s34, s34, s2
	s_lshl_b32 s2, s40, 7
	s_add_u32 s34, s34, s2
	s_add_u32 s42, s42, s34
	s_addc_u32 s43, s43, 0
	v_lshl_add_u32 v13, v2, s36, v10
	v_lshl_add_u32 v14, v3, s36, v10
	v_lshl_add_u32 v15, v4, s36, v10
	v_lshl_add_u32 v16, v5, s36, v10
	v_lshl_add_u32 v17, v6, s36, v10
	v_lshl_add_u32 v18, v7, s36, v10
	v_lshl_add_u32 v19, v8, s36, v10
	v_lshl_add_u32 v20, v9, s36, v10
	global_load_dwordx4 v[144:147], v13, s[42:43]
	global_load_dwordx4 v[148:151], v14, s[42:43]
	global_load_dwordx4 v[152:155], v15, s[42:43]
	global_load_dwordx4 v[156:159], v16, s[42:43]
	global_load_dwordx4 v[160:163], v17, s[42:43]
	global_load_dwordx4 v[164:167], v18, s[42:43]
	global_load_dwordx4 v[168:171], v19, s[42:43]
	global_load_dwordx4 v[172:175], v20, s[42:43]
	s_waitcnt vmcnt(24)
	s_add_u32 s38, s24, 0
	s_sub_u32 s2, s38, 0x10400
	s_cmp_ge_u32 s38, 0x10400
	s_cselect_b32 s3, s2, s38
	s_cselect_b32 s6, 1, 0
	s_cmp_ge_u32 s3, 0x8200
	s_cselect_b32 s7, 1, 0
	s_mul_i32 s2, s7, 0x8200
	s_sub_u32 s3, s3, s2
	s_lshr_b32 s34, s3, 9
	s_and_b32 s3, s3, 0x1ff
	s_cmp_eq_u32 s6, 1
	s_cselect_b32 s35, 7, 5
	s_cselect_b32 s45, 63, 15
	s_lshr_b32 s2, s3, s35
	s_lshl_b32 s2, s2, 1
	s_and_b32 s39, s3, 1
	s_or_b32 s39, s2, s39
	s_lshr_b32 s2, s3, 1
	s_and_b32 s40, s2, s45
	s_cmp_eq_u32 s6, 1
	s_cselect_b32 s35, 20, 21
	s_cselect_b32 s36, 0, 2
	s_cselect_b32 s41, 0, 0x800000
	s_cselect_b32 s2, 0x10400000, 0
	s_lshl_b32 s37, 0x200, s36
	s_add_u32 s41, s41, 0x42000000
	s_add_u32 s2, s2, 0x2400000
	s_lshl_b32 s34, s34, s35
	s_add_u32 s34, s34, s2
	s_lshr_b32 s2, s40, 2
	s_lshl_b32 s2, s2, 8
	s_lshl_b32 s3, s7, 7
	s_add_u32 s2, s2, s3
	s_and_b32 s3, s40, 3
	s_lshl_b32 s3, s3, 5
	s_add_u32 s2, s2, s3
	s_lshl_b32 s2, s2, 11
	s_lshl_b32 s3, s40, 14
	s_cmp_eq_u32 s6, 1
	s_cselect_b32 s2, s3, s2
	s_add_u32 s34, s34, s2
	s_lshl_b32 s2, s39, 6
	s_add_u32 s34, s34, s2
	s_add_u32 s30, s10, s34
	s_addc_u32 s31, s11, 0
	v_lshl_add_u32 v21, v11, s36, v12
	s_lshl_b32 s2, s37, 1
	s_add_u32 s3, s2, s37
	v_add_u32_e32 v22, s37, v21
	v_add_u32_e32 v23, s2, v21
	v_add_u32_e32 v24, s3, v21
	v_mul_f32_e32 v36, s41, v48
	v_mul_f32_e32 v37, s41, v52
	v_mul_f32_e32 v38, s41, v56
	v_mul_f32_e32 v39, s41, v60
	v_mul_f32_e32 v40, s41, v64
	v_mul_f32_e32 v41, s41, v68
	v_mul_f32_e32 v42, s41, v72
	v_mul_f32_e32 v43, s41, v76
	v_med3_f32 v36, v36, s27, v1
	v_med3_f32 v37, v37, s27, v1
	v_med3_f32 v38, v38, s27, v1
	v_med3_f32 v39, v39, s27, v1
	v_med3_f32 v40, v40, s27, v1
	v_med3_f32 v41, v41, s27, v1
	v_med3_f32 v42, v42, s27, v1
	v_med3_f32 v43, v43, s27, v1
	v_cvt_pk_fp8_f32 v28, v36, v37
	v_cvt_pk_fp8_f32 v29, v40, v41
	v_cvt_pk_fp8_f32 v28, v38, v39 op_sel:[0,0,1]
	v_cvt_pk_fp8_f32 v29, v42, v43 op_sel:[0,0,1]
	s_nop 0
	global_store_dwordx2 v21, v[28:29], s[30:31]
	v_mul_f32_e32 v36, s41, v49
	v_mul_f32_e32 v37, s41, v53
	v_mul_f32_e32 v38, s41, v57
	v_mul_f32_e32 v39, s41, v61
	v_mul_f32_e32 v40, s41, v65
	v_mul_f32_e32 v41, s41, v69
	v_mul_f32_e32 v42, s41, v73
	v_mul_f32_e32 v43, s41, v77
	v_med3_f32 v36, v36, s27, v1
	v_med3_f32 v37, v37, s27, v1
	v_med3_f32 v38, v38, s27, v1
	v_med3_f32 v39, v39, s27, v1
	v_med3_f32 v40, v40, s27, v1
	v_med3_f32 v41, v41, s27, v1
	v_med3_f32 v42, v42, s27, v1
	v_med3_f32 v43, v43, s27, v1
	v_cvt_pk_fp8_f32 v30, v36, v37
	v_cvt_pk_fp8_f32 v31, v40, v41
	v_cvt_pk_fp8_f32 v30, v38, v39 op_sel:[0,0,1]
	v_cvt_pk_fp8_f32 v31, v42, v43 op_sel:[0,0,1]
	s_nop 0
	global_store_dwordx2 v22, v[30:31], s[30:31]
	v_mul_f32_e32 v36, s41, v50
	v_mul_f32_e32 v37, s41, v54
	v_mul_f32_e32 v38, s41, v58
	v_mul_f32_e32 v39, s41, v62
	v_mul_f32_e32 v40, s41, v66
	v_mul_f32_e32 v41, s41, v70
	v_mul_f32_e32 v42, s41, v74
	v_mul_f32_e32 v43, s41, v78
	v_med3_f32 v36, v36, s27, v1
	v_med3_f32 v37, v37, s27, v1
	v_med3_f32 v38, v38, s27, v1
	v_med3_f32 v39, v39, s27, v1
	v_med3_f32 v40, v40, s27, v1
	v_med3_f32 v41, v41, s27, v1
	v_med3_f32 v42, v42, s27, v1
	v_med3_f32 v43, v43, s27, v1
	v_cvt_pk_fp8_f32 v32, v36, v37
	v_cvt_pk_fp8_f32 v33, v40, v41
	v_cvt_pk_fp8_f32 v32, v38, v39 op_sel:[0,0,1]
	v_cvt_pk_fp8_f32 v33, v42, v43 op_sel:[0,0,1]
	s_nop 0
	global_store_dwordx2 v23, v[32:33], s[30:31]
	v_mul_f32_e32 v36, s41, v51
	v_mul_f32_e32 v37, s41, v55
	v_mul_f32_e32 v38, s41, v59
	v_mul_f32_e32 v39, s41, v63
	v_mul_f32_e32 v40, s41, v67
	v_mul_f32_e32 v41, s41, v71
	v_mul_f32_e32 v42, s41, v75
	v_mul_f32_e32 v43, s41, v79
	v_med3_f32 v36, v36, s27, v1
	v_med3_f32 v37, v37, s27, v1
	v_med3_f32 v38, v38, s27, v1
	v_med3_f32 v39, v39, s27, v1
	v_med3_f32 v40, v40, s27, v1
	v_med3_f32 v41, v41, s27, v1
	v_med3_f32 v42, v42, s27, v1
	v_med3_f32 v43, v43, s27, v1
	v_cvt_pk_fp8_f32 v34, v36, v37
	v_cvt_pk_fp8_f32 v35, v40, v41
	v_cvt_pk_fp8_f32 v34, v38, v39 op_sel:[0,0,1]
	v_cvt_pk_fp8_f32 v35, v42, v43 op_sel:[0,0,1]
	s_nop 0
	global_store_dwordx2 v24, v[34:35], s[30:31]
	s_add_u32 s38, s24, 4
	s_sub_u32 s2, s38, 0x10400
	s_cmp_ge_u32 s38, 0x10400
	s_cselect_b32 s3, s2, s38
	s_cselect_b32 s6, 1, 0
	s_cmp_ge_u32 s3, 0x8200
	s_cselect_b32 s7, 1, 0
	s_mul_i32 s2, s7, 0x8200
	s_sub_u32 s3, s3, s2
	s_lshr_b32 s34, s3, 9
	s_and_b32 s3, s3, 0x1ff
	s_cmp_eq_u32 s6, 1
	s_cselect_b32 s35, 7, 5
	s_cselect_b32 s45, 63, 15
	s_lshr_b32 s2, s3, s35
	s_lshl_b32 s2, s2, 1
	s_and_b32 s39, s3, 1
	s_or_b32 s39, s2, s39
	s_lshr_b32 s2, s3, 1
	s_and_b32 s40, s2, s45
	s_cmp_eq_u32 s7, 1
	s_cselect_b64 s[44:45], s[14:15], s[12:13]
	s_cselect_b64 s[2:3], s[20:21], s[18:19]
	s_cmp_eq_u32 s6, 1
	s_cselect_b64 s[44:45], s[16:17], s[44:45]
	s_cselect_b64 s[2:3], s[22:23], s[2:3]
	s_cselect_b32 s35, 19, 17
	s_cselect_b32 s36, 2, 0
	s_cmp_lt_u32 s34, 64
	s_cselect_b64 s[28:29], s[44:45], s[2:3]
	s_cselect_b32 s34, s34, 0
	s_lshl_b32 s34, s34, 22
	s_lshl_b32 s2, s39, s35
	s_add_u32 s34, s34, s2
	s_lshl_b32 s2, s40, 7
	s_add_u32 s34, s34, s2
	s_add_u32 s28, s28, s34
	s_addc_u32 s29, s29, 0
	v_lshl_add_u32 v13, v2, s36, v10
	v_lshl_add_u32 v14, v3, s36, v10
	v_lshl_add_u32 v15, v4, s36, v10
	v_lshl_add_u32 v16, v5, s36, v10
	v_lshl_add_u32 v17, v6, s36, v10
	v_lshl_add_u32 v18, v7, s36, v10
	v_lshl_add_u32 v19, v8, s36, v10
	v_lshl_add_u32 v20, v9, s36, v10
	global_load_dwordx4 v[48:51], v13, s[28:29]
	global_load_dwordx4 v[52:55], v14, s[28:29]
	global_load_dwordx4 v[56:59], v15, s[28:29]
	global_load_dwordx4 v[60:63], v16, s[28:29]
	global_load_dwordx4 v[64:67], v17, s[28:29]
	global_load_dwordx4 v[68:71], v18, s[28:29]
	global_load_dwordx4 v[72:75], v19, s[28:29]
	global_load_dwordx4 v[76:79], v20, s[28:29]
	s_waitcnt vmcnt(28)
	s_add_u32 s38, s24, 1
	s_sub_u32 s2, s38, 0x10400
	s_cmp_ge_u32 s38, 0x10400
	s_cselect_b32 s3, s2, s38
	s_cselect_b32 s6, 1, 0
	s_cmp_ge_u32 s3, 0x8200
	s_cselect_b32 s7, 1, 0
	s_mul_i32 s2, s7, 0x8200
	s_sub_u32 s3, s3, s2
	s_lshr_b32 s34, s3, 9
	s_and_b32 s3, s3, 0x1ff
	s_cmp_eq_u32 s6, 1
	s_cselect_b32 s35, 7, 5
	s_cselect_b32 s45, 63, 15
	s_lshr_b32 s2, s3, s35
	s_lshl_b32 s2, s2, 1
	s_and_b32 s39, s3, 1
	s_or_b32 s39, s2, s39
	s_lshr_b32 s2, s3, 1
	s_and_b32 s40, s2, s45
	s_cmp_eq_u32 s6, 1
	s_cselect_b32 s35, 20, 21
	s_cselect_b32 s36, 0, 2
	s_cselect_b32 s41, 0, 0x800000
	s_cselect_b32 s2, 0x10400000, 0
	s_lshl_b32 s37, 0x200, s36
	s_add_u32 s41, s41, 0x42000000
	s_add_u32 s2, s2, 0x2400000
	s_lshl_b32 s34, s34, s35
	s_add_u32 s34, s34, s2
	s_lshr_b32 s2, s40, 2
	s_lshl_b32 s2, s2, 8
	s_lshl_b32 s3, s7, 7
	s_add_u32 s2, s2, s3
	s_and_b32 s3, s40, 3
	s_lshl_b32 s3, s3, 5
	s_add_u32 s2, s2, s3
	s_lshl_b32 s2, s2, 11
	s_lshl_b32 s3, s40, 14
	s_cmp_eq_u32 s6, 1
	s_cselect_b32 s2, s3, s2
	s_add_u32 s34, s34, s2
	s_lshl_b32 s2, s39, 6
	s_add_u32 s34, s34, s2
	s_add_u32 s30, s10, s34
	s_addc_u32 s31, s11, 0
	v_lshl_add_u32 v21, v11, s36, v12
	s_lshl_b32 s2, s37, 1
	s_add_u32 s3, s2, s37
	v_add_u32_e32 v22, s37, v21
	v_add_u32_e32 v23, s2, v21
	v_add_u32_e32 v24, s3, v21
	v_mul_f32_e32 v36, s41, v80
	v_mul_f32_e32 v37, s41, v84
	v_mul_f32_e32 v38, s41, v88
	v_mul_f32_e32 v39, s41, v92
	v_mul_f32_e32 v40, s41, v96
	v_mul_f32_e32 v41, s41, v100
	v_mul_f32_e32 v42, s41, v104
	v_mul_f32_e32 v43, s41, v108
	v_med3_f32 v36, v36, s27, v1
	v_med3_f32 v37, v37, s27, v1
	v_med3_f32 v38, v38, s27, v1
	v_med3_f32 v39, v39, s27, v1
	v_med3_f32 v40, v40, s27, v1
	v_med3_f32 v41, v41, s27, v1
	v_med3_f32 v42, v42, s27, v1
	v_med3_f32 v43, v43, s27, v1
	v_cvt_pk_fp8_f32 v28, v36, v37
	v_cvt_pk_fp8_f32 v29, v40, v41
	v_cvt_pk_fp8_f32 v28, v38, v39 op_sel:[0,0,1]
	v_cvt_pk_fp8_f32 v29, v42, v43 op_sel:[0,0,1]
	s_nop 0
	global_store_dwordx2 v21, v[28:29], s[30:31]
	v_mul_f32_e32 v36, s41, v81
	v_mul_f32_e32 v37, s41, v85
	v_mul_f32_e32 v38, s41, v89
	v_mul_f32_e32 v39, s41, v93
	v_mul_f32_e32 v40, s41, v97
	v_mul_f32_e32 v41, s41, v101
	v_mul_f32_e32 v42, s41, v105
	v_mul_f32_e32 v43, s41, v109
	v_med3_f32 v36, v36, s27, v1
	v_med3_f32 v37, v37, s27, v1
	v_med3_f32 v38, v38, s27, v1
	v_med3_f32 v39, v39, s27, v1
	v_med3_f32 v40, v40, s27, v1
	v_med3_f32 v41, v41, s27, v1
	v_med3_f32 v42, v42, s27, v1
	v_med3_f32 v43, v43, s27, v1
	v_cvt_pk_fp8_f32 v30, v36, v37
	v_cvt_pk_fp8_f32 v31, v40, v41
	v_cvt_pk_fp8_f32 v30, v38, v39 op_sel:[0,0,1]
	v_cvt_pk_fp8_f32 v31, v42, v43 op_sel:[0,0,1]
	s_nop 0
	global_store_dwordx2 v22, v[30:31], s[30:31]
	v_mul_f32_e32 v36, s41, v82
	v_mul_f32_e32 v37, s41, v86
	v_mul_f32_e32 v38, s41, v90
	v_mul_f32_e32 v39, s41, v94
	v_mul_f32_e32 v40, s41, v98
	v_mul_f32_e32 v41, s41, v102
	v_mul_f32_e32 v42, s41, v106
	v_mul_f32_e32 v43, s41, v110
	v_med3_f32 v36, v36, s27, v1
	v_med3_f32 v37, v37, s27, v1
	v_med3_f32 v38, v38, s27, v1
	v_med3_f32 v39, v39, s27, v1
	v_med3_f32 v40, v40, s27, v1
	v_med3_f32 v41, v41, s27, v1
	v_med3_f32 v42, v42, s27, v1
	v_med3_f32 v43, v43, s27, v1
	v_cvt_pk_fp8_f32 v32, v36, v37
	v_cvt_pk_fp8_f32 v33, v40, v41
	v_cvt_pk_fp8_f32 v32, v38, v39 op_sel:[0,0,1]
	v_cvt_pk_fp8_f32 v33, v42, v43 op_sel:[0,0,1]
	s_nop 0
	global_store_dwordx2 v23, v[32:33], s[30:31]
	v_mul_f32_e32 v36, s41, v83
	v_mul_f32_e32 v37, s41, v87
	v_mul_f32_e32 v38, s41, v91
	v_mul_f32_e32 v39, s41, v95
	v_mul_f32_e32 v40, s41, v99
	v_mul_f32_e32 v41, s41, v103
	v_mul_f32_e32 v42, s41, v107
	v_mul_f32_e32 v43, s41, v111
	v_med3_f32 v36, v36, s27, v1
	v_med3_f32 v37, v37, s27, v1
	v_med3_f32 v38, v38, s27, v1
	v_med3_f32 v39, v39, s27, v1
	v_med3_f32 v40, v40, s27, v1
	v_med3_f32 v41, v41, s27, v1
	v_med3_f32 v42, v42, s27, v1
	v_med3_f32 v43, v43, s27, v1
	v_cvt_pk_fp8_f32 v34, v36, v37
	v_cvt_pk_fp8_f32 v35, v40, v41
	v_cvt_pk_fp8_f32 v34, v38, v39 op_sel:[0,0,1]
	v_cvt_pk_fp8_f32 v35, v42, v43 op_sel:[0,0,1]
	s_nop 0
	global_store_dwordx2 v24, v[34:35], s[30:31]
	s_add_u32 s38, s24, 5
	s_sub_u32 s2, s38, 0x10400
	s_cmp_ge_u32 s38, 0x10400
	s_cselect_b32 s3, s2, s38
	s_cselect_b32 s6, 1, 0
	s_cmp_ge_u32 s3, 0x8200
	s_cselect_b32 s7, 1, 0
	s_mul_i32 s2, s7, 0x8200
	s_sub_u32 s3, s3, s2
	s_lshr_b32 s34, s3, 9
	s_and_b32 s3, s3, 0x1ff
	s_cmp_eq_u32 s6, 1
	s_cselect_b32 s35, 7, 5
	s_cselect_b32 s45, 63, 15
	s_lshr_b32 s2, s3, s35
	s_lshl_b32 s2, s2, 1
	s_and_b32 s39, s3, 1
	s_or_b32 s39, s2, s39
	s_lshr_b32 s2, s3, 1
	s_and_b32 s40, s2, s45
	s_cmp_eq_u32 s7, 1
	s_cselect_b64 s[44:45], s[14:15], s[12:13]
	s_cselect_b64 s[2:3], s[20:21], s[18:19]
	s_cmp_eq_u32 s6, 1
	s_cselect_b64 s[44:45], s[16:17], s[44:45]
	s_cselect_b64 s[2:3], s[22:23], s[2:3]
	s_cselect_b32 s35, 19, 17
	s_cselect_b32 s36, 2, 0
	s_cmp_lt_u32 s34, 64
	s_cselect_b64 s[42:43], s[44:45], s[2:3]
	s_cselect_b32 s34, s34, 0
	s_lshl_b32 s34, s34, 22
	s_lshl_b32 s2, s39, s35
	s_add_u32 s34, s34, s2
	s_lshl_b32 s2, s40, 7
	s_add_u32 s34, s34, s2
	s_add_u32 s42, s42, s34
	s_addc_u32 s43, s43, 0
	v_lshl_add_u32 v13, v2, s36, v10
	v_lshl_add_u32 v14, v3, s36, v10
	v_lshl_add_u32 v15, v4, s36, v10
	v_lshl_add_u32 v16, v5, s36, v10
	v_lshl_add_u32 v17, v6, s36, v10
	v_lshl_add_u32 v18, v7, s36, v10
	v_lshl_add_u32 v19, v8, s36, v10
	v_lshl_add_u32 v20, v9, s36, v10
	global_load_dwordx4 v[80:83], v13, s[42:43]
	global_load_dwordx4 v[84:87], v14, s[42:43]
	global_load_dwordx4 v[88:91], v15, s[42:43]
	global_load_dwordx4 v[92:95], v16, s[42:43]
	global_load_dwordx4 v[96:99], v17, s[42:43]
	global_load_dwordx4 v[100:103], v18, s[42:43]
	global_load_dwordx4 v[104:107], v19, s[42:43]
	global_load_dwordx4 v[108:111], v20, s[42:43]
	s_waitcnt vmcnt(32)
	s_add_u32 s38, s24, 2
	s_sub_u32 s2, s38, 0x10400
	s_cmp_ge_u32 s38, 0x10400
	s_cselect_b32 s3, s2, s38
	s_cselect_b32 s6, 1, 0
	s_cmp_ge_u32 s3, 0x8200
	s_cselect_b32 s7, 1, 0
	s_mul_i32 s2, s7, 0x8200
	s_sub_u32 s3, s3, s2
	s_lshr_b32 s34, s3, 9
	s_and_b32 s3, s3, 0x1ff
	s_cmp_eq_u32 s6, 1
	s_cselect_b32 s35, 7, 5
	s_cselect_b32 s45, 63, 15
	s_lshr_b32 s2, s3, s35
	s_lshl_b32 s2, s2, 1
	s_and_b32 s39, s3, 1
	s_or_b32 s39, s2, s39
	s_lshr_b32 s2, s3, 1
	s_and_b32 s40, s2, s45
	s_cmp_eq_u32 s6, 1
	s_cselect_b32 s35, 20, 21
	s_cselect_b32 s36, 0, 2
	s_cselect_b32 s41, 0, 0x800000
	s_cselect_b32 s2, 0x10400000, 0
	s_lshl_b32 s37, 0x200, s36
	s_add_u32 s41, s41, 0x42000000
	s_add_u32 s2, s2, 0x2400000
	s_lshl_b32 s34, s34, s35
	s_add_u32 s34, s34, s2
	s_lshr_b32 s2, s40, 2
	s_lshl_b32 s2, s2, 8
	s_lshl_b32 s3, s7, 7
	s_add_u32 s2, s2, s3
	s_and_b32 s3, s40, 3
	s_lshl_b32 s3, s3, 5
	s_add_u32 s2, s2, s3
	s_lshl_b32 s2, s2, 11
	s_lshl_b32 s3, s40, 14
	s_cmp_eq_u32 s6, 1
	s_cselect_b32 s2, s3, s2
	s_add_u32 s34, s34, s2
	s_lshl_b32 s2, s39, 6
	s_add_u32 s34, s34, s2
	s_add_u32 s30, s10, s34
	s_addc_u32 s31, s11, 0
	v_lshl_add_u32 v21, v11, s36, v12
	s_lshl_b32 s2, s37, 1
	s_add_u32 s3, s2, s37
	v_add_u32_e32 v22, s37, v21
	v_add_u32_e32 v23, s2, v21
	v_add_u32_e32 v24, s3, v21
	v_mul_f32_e32 v36, s41, v112
	v_mul_f32_e32 v37, s41, v116
	v_mul_f32_e32 v38, s41, v120
	v_mul_f32_e32 v39, s41, v124
	v_mul_f32_e32 v40, s41, v128
	v_mul_f32_e32 v41, s41, v132
	v_mul_f32_e32 v42, s41, v136
	v_mul_f32_e32 v43, s41, v140
	v_med3_f32 v36, v36, s27, v1
	v_med3_f32 v37, v37, s27, v1
	v_med3_f32 v38, v38, s27, v1
	v_med3_f32 v39, v39, s27, v1
	v_med3_f32 v40, v40, s27, v1
	v_med3_f32 v41, v41, s27, v1
	v_med3_f32 v42, v42, s27, v1
	v_med3_f32 v43, v43, s27, v1
	v_cvt_pk_fp8_f32 v28, v36, v37
	v_cvt_pk_fp8_f32 v29, v40, v41
	v_cvt_pk_fp8_f32 v28, v38, v39 op_sel:[0,0,1]
	v_cvt_pk_fp8_f32 v29, v42, v43 op_sel:[0,0,1]
	s_nop 0
	global_store_dwordx2 v21, v[28:29], s[30:31]
	v_mul_f32_e32 v36, s41, v113
	v_mul_f32_e32 v37, s41, v117
	v_mul_f32_e32 v38, s41, v121
	v_mul_f32_e32 v39, s41, v125
	v_mul_f32_e32 v40, s41, v129
	v_mul_f32_e32 v41, s41, v133
	v_mul_f32_e32 v42, s41, v137
	v_mul_f32_e32 v43, s41, v141
	v_med3_f32 v36, v36, s27, v1
	v_med3_f32 v37, v37, s27, v1
	v_med3_f32 v38, v38, s27, v1
	v_med3_f32 v39, v39, s27, v1
	v_med3_f32 v40, v40, s27, v1
	v_med3_f32 v41, v41, s27, v1
	v_med3_f32 v42, v42, s27, v1
	v_med3_f32 v43, v43, s27, v1
	v_cvt_pk_fp8_f32 v30, v36, v37
	v_cvt_pk_fp8_f32 v31, v40, v41
	v_cvt_pk_fp8_f32 v30, v38, v39 op_sel:[0,0,1]
	v_cvt_pk_fp8_f32 v31, v42, v43 op_sel:[0,0,1]
	s_nop 0
	global_store_dwordx2 v22, v[30:31], s[30:31]
	v_mul_f32_e32 v36, s41, v114
	v_mul_f32_e32 v37, s41, v118
	v_mul_f32_e32 v38, s41, v122
	v_mul_f32_e32 v39, s41, v126
	v_mul_f32_e32 v40, s41, v130
	v_mul_f32_e32 v41, s41, v134
	v_mul_f32_e32 v42, s41, v138
	v_mul_f32_e32 v43, s41, v142
	v_med3_f32 v36, v36, s27, v1
	v_med3_f32 v37, v37, s27, v1
	v_med3_f32 v38, v38, s27, v1
	v_med3_f32 v39, v39, s27, v1
	v_med3_f32 v40, v40, s27, v1
	v_med3_f32 v41, v41, s27, v1
	v_med3_f32 v42, v42, s27, v1
	v_med3_f32 v43, v43, s27, v1
	v_cvt_pk_fp8_f32 v32, v36, v37
	v_cvt_pk_fp8_f32 v33, v40, v41
	v_cvt_pk_fp8_f32 v32, v38, v39 op_sel:[0,0,1]
	v_cvt_pk_fp8_f32 v33, v42, v43 op_sel:[0,0,1]
	s_nop 0
	global_store_dwordx2 v23, v[32:33], s[30:31]
	v_mul_f32_e32 v36, s41, v115
	v_mul_f32_e32 v37, s41, v119
	v_mul_f32_e32 v38, s41, v123
	v_mul_f32_e32 v39, s41, v127
	v_mul_f32_e32 v40, s41, v131
	v_mul_f32_e32 v41, s41, v135
	v_mul_f32_e32 v42, s41, v139
	v_mul_f32_e32 v43, s41, v143
	v_med3_f32 v36, v36, s27, v1
	v_med3_f32 v37, v37, s27, v1
	v_med3_f32 v38, v38, s27, v1
	v_med3_f32 v39, v39, s27, v1
	v_med3_f32 v40, v40, s27, v1
	v_med3_f32 v41, v41, s27, v1
	v_med3_f32 v42, v42, s27, v1
	v_med3_f32 v43, v43, s27, v1
	v_cvt_pk_fp8_f32 v34, v36, v37
	v_cvt_pk_fp8_f32 v35, v40, v41
	v_cvt_pk_fp8_f32 v34, v38, v39 op_sel:[0,0,1]
	v_cvt_pk_fp8_f32 v35, v42, v43 op_sel:[0,0,1]
	s_nop 0
	global_store_dwordx2 v24, v[34:35], s[30:31]
	s_add_u32 s38, s24, 6
	s_sub_u32 s2, s38, 0x10400
	s_cmp_ge_u32 s38, 0x10400
	s_cselect_b32 s3, s2, s38
	s_cselect_b32 s6, 1, 0
	s_cmp_ge_u32 s3, 0x8200
	s_cselect_b32 s7, 1, 0
	s_mul_i32 s2, s7, 0x8200
	s_sub_u32 s3, s3, s2
	s_lshr_b32 s34, s3, 9
	s_and_b32 s3, s3, 0x1ff
	s_cmp_eq_u32 s6, 1
	s_cselect_b32 s35, 7, 5
	s_cselect_b32 s45, 63, 15
	s_lshr_b32 s2, s3, s35
	s_lshl_b32 s2, s2, 1
	s_and_b32 s39, s3, 1
	s_or_b32 s39, s2, s39
	s_lshr_b32 s2, s3, 1
	s_and_b32 s40, s2, s45
	s_cmp_eq_u32 s7, 1
	s_cselect_b64 s[44:45], s[14:15], s[12:13]
	s_cselect_b64 s[2:3], s[20:21], s[18:19]
	s_cmp_eq_u32 s6, 1
	s_cselect_b64 s[44:45], s[16:17], s[44:45]
	s_cselect_b64 s[2:3], s[22:23], s[2:3]
	s_cselect_b32 s35, 19, 17
	s_cselect_b32 s36, 2, 0
	s_cmp_lt_u32 s34, 64
	s_cselect_b64 s[28:29], s[44:45], s[2:3]
	s_cselect_b32 s34, s34, 0
	s_lshl_b32 s34, s34, 22
	s_lshl_b32 s2, s39, s35
	s_add_u32 s34, s34, s2
	s_lshl_b32 s2, s40, 7
	s_add_u32 s34, s34, s2
	s_add_u32 s28, s28, s34
	s_addc_u32 s29, s29, 0
	v_lshl_add_u32 v13, v2, s36, v10
	v_lshl_add_u32 v14, v3, s36, v10
	v_lshl_add_u32 v15, v4, s36, v10
	v_lshl_add_u32 v16, v5, s36, v10
	v_lshl_add_u32 v17, v6, s36, v10
	v_lshl_add_u32 v18, v7, s36, v10
	v_lshl_add_u32 v19, v8, s36, v10
	v_lshl_add_u32 v20, v9, s36, v10
	global_load_dwordx4 v[112:115], v13, s[28:29]
	global_load_dwordx4 v[116:119], v14, s[28:29]
	global_load_dwordx4 v[120:123], v15, s[28:29]
	global_load_dwordx4 v[124:127], v16, s[28:29]
	global_load_dwordx4 v[128:131], v17, s[28:29]
	global_load_dwordx4 v[132:135], v18, s[28:29]
	global_load_dwordx4 v[136:139], v19, s[28:29]
	global_load_dwordx4 v[140:143], v20, s[28:29]
	s_waitcnt vmcnt(36)
	s_add_u32 s38, s24, 3
	s_sub_u32 s2, s38, 0x10400
	s_cmp_ge_u32 s38, 0x10400
	s_cselect_b32 s3, s2, s38
	s_cselect_b32 s6, 1, 0
	s_cmp_ge_u32 s3, 0x8200
	s_cselect_b32 s7, 1, 0
	s_mul_i32 s2, s7, 0x8200
	s_sub_u32 s3, s3, s2
	s_lshr_b32 s34, s3, 9
	s_and_b32 s3, s3, 0x1ff
	s_cmp_eq_u32 s6, 1
	s_cselect_b32 s35, 7, 5
	s_cselect_b32 s45, 63, 15
	s_lshr_b32 s2, s3, s35
	s_lshl_b32 s2, s2, 1
	s_and_b32 s39, s3, 1
	s_or_b32 s39, s2, s39
	s_lshr_b32 s2, s3, 1
	s_and_b32 s40, s2, s45
	s_cmp_eq_u32 s6, 1
	s_cselect_b32 s35, 20, 21
	s_cselect_b32 s36, 0, 2
	s_cselect_b32 s41, 0, 0x800000
	s_cselect_b32 s2, 0x10400000, 0
	s_lshl_b32 s37, 0x200, s36
	s_add_u32 s41, s41, 0x42000000
	s_add_u32 s2, s2, 0x2400000
	s_lshl_b32 s34, s34, s35
	s_add_u32 s34, s34, s2
	s_lshr_b32 s2, s40, 2
	s_lshl_b32 s2, s2, 8
	s_lshl_b32 s3, s7, 7
	s_add_u32 s2, s2, s3
	s_and_b32 s3, s40, 3
	s_lshl_b32 s3, s3, 5
	s_add_u32 s2, s2, s3
	s_lshl_b32 s2, s2, 11
	s_lshl_b32 s3, s40, 14
	s_cmp_eq_u32 s6, 1
	s_cselect_b32 s2, s3, s2
	s_add_u32 s34, s34, s2
	s_lshl_b32 s2, s39, 6
	s_add_u32 s34, s34, s2
	s_add_u32 s30, s10, s34
	s_addc_u32 s31, s11, 0
	v_lshl_add_u32 v21, v11, s36, v12
	s_lshl_b32 s2, s37, 1
	s_add_u32 s3, s2, s37
	v_add_u32_e32 v22, s37, v21
	v_add_u32_e32 v23, s2, v21
	v_add_u32_e32 v24, s3, v21
	v_mul_f32_e32 v36, s41, v144
	v_mul_f32_e32 v37, s41, v148
	v_mul_f32_e32 v38, s41, v152
	v_mul_f32_e32 v39, s41, v156
	v_mul_f32_e32 v40, s41, v160
	v_mul_f32_e32 v41, s41, v164
	v_mul_f32_e32 v42, s41, v168
	v_mul_f32_e32 v43, s41, v172
	v_med3_f32 v36, v36, s27, v1
	v_med3_f32 v37, v37, s27, v1
	v_med3_f32 v38, v38, s27, v1
	v_med3_f32 v39, v39, s27, v1
	v_med3_f32 v40, v40, s27, v1
	v_med3_f32 v41, v41, s27, v1
	v_med3_f32 v42, v42, s27, v1
	v_med3_f32 v43, v43, s27, v1
	v_cvt_pk_fp8_f32 v28, v36, v37
	v_cvt_pk_fp8_f32 v29, v40, v41
	v_cvt_pk_fp8_f32 v28, v38, v39 op_sel:[0,0,1]
	v_cvt_pk_fp8_f32 v29, v42, v43 op_sel:[0,0,1]
	s_nop 0
	global_store_dwordx2 v21, v[28:29], s[30:31]
	v_mul_f32_e32 v36, s41, v145
	v_mul_f32_e32 v37, s41, v149
	v_mul_f32_e32 v38, s41, v153
	v_mul_f32_e32 v39, s41, v157
	v_mul_f32_e32 v40, s41, v161
	v_mul_f32_e32 v41, s41, v165
	v_mul_f32_e32 v42, s41, v169
	v_mul_f32_e32 v43, s41, v173
	v_med3_f32 v36, v36, s27, v1
	v_med3_f32 v37, v37, s27, v1
	v_med3_f32 v38, v38, s27, v1
	v_med3_f32 v39, v39, s27, v1
	v_med3_f32 v40, v40, s27, v1
	v_med3_f32 v41, v41, s27, v1
	v_med3_f32 v42, v42, s27, v1
	v_med3_f32 v43, v43, s27, v1
	v_cvt_pk_fp8_f32 v30, v36, v37
	v_cvt_pk_fp8_f32 v31, v40, v41
	v_cvt_pk_fp8_f32 v30, v38, v39 op_sel:[0,0,1]
	v_cvt_pk_fp8_f32 v31, v42, v43 op_sel:[0,0,1]
	s_nop 0
	global_store_dwordx2 v22, v[30:31], s[30:31]
	v_mul_f32_e32 v36, s41, v146
	v_mul_f32_e32 v37, s41, v150
	v_mul_f32_e32 v38, s41, v154
	v_mul_f32_e32 v39, s41, v158
	v_mul_f32_e32 v40, s41, v162
	v_mul_f32_e32 v41, s41, v166
	v_mul_f32_e32 v42, s41, v170
	v_mul_f32_e32 v43, s41, v174
	v_med3_f32 v36, v36, s27, v1
	v_med3_f32 v37, v37, s27, v1
	v_med3_f32 v38, v38, s27, v1
	v_med3_f32 v39, v39, s27, v1
	v_med3_f32 v40, v40, s27, v1
	v_med3_f32 v41, v41, s27, v1
	v_med3_f32 v42, v42, s27, v1
	v_med3_f32 v43, v43, s27, v1
	v_cvt_pk_fp8_f32 v32, v36, v37
	v_cvt_pk_fp8_f32 v33, v40, v41
	v_cvt_pk_fp8_f32 v32, v38, v39 op_sel:[0,0,1]
	v_cvt_pk_fp8_f32 v33, v42, v43 op_sel:[0,0,1]
	s_nop 0
	global_store_dwordx2 v23, v[32:33], s[30:31]
	v_mul_f32_e32 v36, s41, v147
	v_mul_f32_e32 v37, s41, v151
	v_mul_f32_e32 v38, s41, v155
	v_mul_f32_e32 v39, s41, v159
	v_mul_f32_e32 v40, s41, v163
	v_mul_f32_e32 v41, s41, v167
	v_mul_f32_e32 v42, s41, v171
	v_mul_f32_e32 v43, s41, v175
	v_med3_f32 v36, v36, s27, v1
	v_med3_f32 v37, v37, s27, v1
	v_med3_f32 v38, v38, s27, v1
	v_med3_f32 v39, v39, s27, v1
	v_med3_f32 v40, v40, s27, v1
	v_med3_f32 v41, v41, s27, v1
	v_med3_f32 v42, v42, s27, v1
	v_med3_f32 v43, v43, s27, v1
	v_cvt_pk_fp8_f32 v34, v36, v37
	v_cvt_pk_fp8_f32 v35, v40, v41
	v_cvt_pk_fp8_f32 v34, v38, v39 op_sel:[0,0,1]
	v_cvt_pk_fp8_f32 v35, v42, v43 op_sel:[0,0,1]
	s_nop 0
	global_store_dwordx2 v24, v[34:35], s[30:31]
	s_add_u32 s38, s24, 7
	s_sub_u32 s2, s38, 0x10400
	s_cmp_ge_u32 s38, 0x10400
	s_cselect_b32 s3, s2, s38
	s_cselect_b32 s6, 1, 0
	s_cmp_ge_u32 s3, 0x8200
	s_cselect_b32 s7, 1, 0
	s_mul_i32 s2, s7, 0x8200
	s_sub_u32 s3, s3, s2
	s_lshr_b32 s34, s3, 9
	s_and_b32 s3, s3, 0x1ff
	s_cmp_eq_u32 s6, 1
	s_cselect_b32 s35, 7, 5
	s_cselect_b32 s45, 63, 15
	s_lshr_b32 s2, s3, s35
	s_lshl_b32 s2, s2, 1
	s_and_b32 s39, s3, 1
	s_or_b32 s39, s2, s39
	s_lshr_b32 s2, s3, 1
	s_and_b32 s40, s2, s45
	s_cmp_eq_u32 s7, 1
	s_cselect_b64 s[44:45], s[14:15], s[12:13]
	s_cselect_b64 s[2:3], s[20:21], s[18:19]
	s_cmp_eq_u32 s6, 1
	s_cselect_b64 s[44:45], s[16:17], s[44:45]
	s_cselect_b64 s[2:3], s[22:23], s[2:3]
	s_cselect_b32 s35, 19, 17
	s_cselect_b32 s36, 2, 0
	s_cmp_lt_u32 s34, 64
	s_cselect_b64 s[42:43], s[44:45], s[2:3]
	s_cselect_b32 s34, s34, 0
	s_lshl_b32 s34, s34, 22
	s_lshl_b32 s2, s39, s35
	s_add_u32 s34, s34, s2
	s_lshl_b32 s2, s40, 7
	s_add_u32 s34, s34, s2
	s_add_u32 s42, s42, s34
	s_addc_u32 s43, s43, 0
	v_lshl_add_u32 v13, v2, s36, v10
	v_lshl_add_u32 v14, v3, s36, v10
	v_lshl_add_u32 v15, v4, s36, v10
	v_lshl_add_u32 v16, v5, s36, v10
	v_lshl_add_u32 v17, v6, s36, v10
	v_lshl_add_u32 v18, v7, s36, v10
	v_lshl_add_u32 v19, v8, s36, v10
	v_lshl_add_u32 v20, v9, s36, v10
	global_load_dwordx4 v[144:147], v13, s[42:43]
	global_load_dwordx4 v[148:151], v14, s[42:43]
	global_load_dwordx4 v[152:155], v15, s[42:43]
	global_load_dwordx4 v[156:159], v16, s[42:43]
	global_load_dwordx4 v[160:163], v17, s[42:43]
	global_load_dwordx4 v[164:167], v18, s[42:43]
	global_load_dwordx4 v[168:171], v19, s[42:43]
	global_load_dwordx4 v[172:175], v20, s[42:43]
	s_mov_b32 s26, 4
.Lcv_steady:
	s_add_u32 s2, s26, 8
	s_cmp_gt_u32 s2, s25
	s_cbranch_scc1 .Lcv_drain
	s_waitcnt vmcnt(36)
	s_add_u32 s38, s24, s26
	s_sub_u32 s2, s38, 0x10400
	s_cmp_ge_u32 s38, 0x10400
	s_cselect_b32 s3, s2, s38
	s_cselect_b32 s6, 1, 0
	s_cmp_ge_u32 s3, 0x8200
	s_cselect_b32 s7, 1, 0
	s_mul_i32 s2, s7, 0x8200
	s_sub_u32 s3, s3, s2
	s_lshr_b32 s34, s3, 9
	s_and_b32 s3, s3, 0x1ff
	s_cmp_eq_u32 s6, 1
	s_cselect_b32 s35, 7, 5
	s_cselect_b32 s45, 63, 15
	s_lshr_b32 s2, s3, s35
	s_lshl_b32 s2, s2, 1
	s_and_b32 s39, s3, 1
	s_or_b32 s39, s2, s39
	s_lshr_b32 s2, s3, 1
	s_and_b32 s40, s2, s45
	s_cmp_eq_u32 s6, 1
	s_cselect_b32 s35, 20, 21
	s_cselect_b32 s36, 0, 2
	s_cselect_b32 s41, 0, 0x800000
	s_cselect_b32 s2, 0x10400000, 0
	s_lshl_b32 s37, 0x200, s36
	s_add_u32 s41, s41, 0x42000000
	s_add_u32 s2, s2, 0x2400000
	s_lshl_b32 s34, s34, s35
	s_add_u32 s34, s34, s2
	s_lshr_b32 s2, s40, 2
	s_lshl_b32 s2, s2, 8
	s_lshl_b32 s3, s7, 7
	s_add_u32 s2, s2, s3
	s_and_b32 s3, s40, 3
	s_lshl_b32 s3, s3, 5
	s_add_u32 s2, s2, s3
	s_lshl_b32 s2, s2, 11
	s_lshl_b32 s3, s40, 14
	s_cmp_eq_u32 s6, 1
	s_cselect_b32 s2, s3, s2
	s_add_u32 s34, s34, s2
	s_lshl_b32 s2, s39, 6
	s_add_u32 s34, s34, s2
	s_add_u32 s30, s10, s34
	s_addc_u32 s31, s11, 0
	v_lshl_add_u32 v21, v11, s36, v12
	s_lshl_b32 s2, s37, 1
	s_add_u32 s3, s2, s37
	v_add_u32_e32 v22, s37, v21
	v_add_u32_e32 v23, s2, v21
	v_add_u32_e32 v24, s3, v21
	v_mul_f32_e32 v36, s41, v48
	v_mul_f32_e32 v37, s41, v52
	v_mul_f32_e32 v38, s41, v56
	v_mul_f32_e32 v39, s41, v60
	v_mul_f32_e32 v40, s41, v64
	v_mul_f32_e32 v41, s41, v68
	v_mul_f32_e32 v42, s41, v72
	v_mul_f32_e32 v43, s41, v76
	v_med3_f32 v36, v36, s27, v1
	v_med3_f32 v37, v37, s27, v1
	v_med3_f32 v38, v38, s27, v1
	v_med3_f32 v39, v39, s27, v1
	v_med3_f32 v40, v40, s27, v1
	v_med3_f32 v41, v41, s27, v1
	v_med3_f32 v42, v42, s27, v1
	v_med3_f32 v43, v43, s27, v1
	v_cvt_pk_fp8_f32 v28, v36, v37
	v_cvt_pk_fp8_f32 v29, v40, v41
	v_cvt_pk_fp8_f32 v28, v38, v39 op_sel:[0,0,1]
	v_cvt_pk_fp8_f32 v29, v42, v43 op_sel:[0,0,1]
	s_nop 0
	global_store_dwordx2 v21, v[28:29], s[30:31]
	v_mul_f32_e32 v36, s41, v49
	v_mul_f32_e32 v37, s41, v53
	v_mul_f32_e32 v38, s41, v57
	v_mul_f32_e32 v39, s41, v61
	v_mul_f32_e32 v40, s41, v65
	v_mul_f32_e32 v41, s41, v69
	v_mul_f32_e32 v42, s41, v73
	v_mul_f32_e32 v43, s41, v77
	v_med3_f32 v36, v36, s27, v1
	v_med3_f32 v37, v37, s27, v1
	v_med3_f32 v38, v38, s27, v1
	v_med3_f32 v39, v39, s27, v1
	v_med3_f32 v40, v40, s27, v1
	v_med3_f32 v41, v41, s27, v1
	v_med3_f32 v42, v42, s27, v1
	v_med3_f32 v43, v43, s27, v1
	v_cvt_pk_fp8_f32 v30, v36, v37
	v_cvt_pk_fp8_f32 v31, v40, v41
	v_cvt_pk_fp8_f32 v30, v38, v39 op_sel:[0,0,1]
	v_cvt_pk_fp8_f32 v31, v42, v43 op_sel:[0,0,1]
	s_nop 0
	global_store_dwordx2 v22, v[30:31], s[30:31]
	v_mul_f32_e32 v36, s41, v50
	v_mul_f32_e32 v37, s41, v54
	v_mul_f32_e32 v38, s41, v58
	v_mul_f32_e32 v39, s41, v62
	v_mul_f32_e32 v40, s41, v66
	v_mul_f32_e32 v41, s41, v70
	v_mul_f32_e32 v42, s41, v74
	v_mul_f32_e32 v43, s41, v78
	v_med3_f32 v36, v36, s27, v1
	v_med3_f32 v37, v37, s27, v1
	v_med3_f32 v38, v38, s27, v1
	v_med3_f32 v39, v39, s27, v1
	v_med3_f32 v40, v40, s27, v1
	v_med3_f32 v41, v41, s27, v1
	v_med3_f32 v42, v42, s27, v1
	v_med3_f32 v43, v43, s27, v1
	v_cvt_pk_fp8_f32 v32, v36, v37
	v_cvt_pk_fp8_f32 v33, v40, v41
	v_cvt_pk_fp8_f32 v32, v38, v39 op_sel:[0,0,1]
	v_cvt_pk_fp8_f32 v33, v42, v43 op_sel:[0,0,1]
	s_nop 0
	global_store_dwordx2 v23, v[32:33], s[30:31]
	v_mul_f32_e32 v36, s41, v51
	v_mul_f32_e32 v37, s41, v55
	v_mul_f32_e32 v38, s41, v59
	v_mul_f32_e32 v39, s41, v63
	v_mul_f32_e32 v40, s41, v67
	v_mul_f32_e32 v41, s41, v71
	v_mul_f32_e32 v42, s41, v75
	v_mul_f32_e32 v43, s41, v79
	v_med3_f32 v36, v36, s27, v1
	v_med3_f32 v37, v37, s27, v1
	v_med3_f32 v38, v38, s27, v1
	v_med3_f32 v39, v39, s27, v1
	v_med3_f32 v40, v40, s27, v1
	v_med3_f32 v41, v41, s27, v1
	v_med3_f32 v42, v42, s27, v1
	v_med3_f32 v43, v43, s27, v1
	v_cvt_pk_fp8_f32 v34, v36, v37
	v_cvt_pk_fp8_f32 v35, v40, v41
	v_cvt_pk_fp8_f32 v34, v38, v39 op_sel:[0,0,1]
	v_cvt_pk_fp8_f32 v35, v42, v43 op_sel:[0,0,1]
	s_nop 0
	global_store_dwordx2 v24, v[34:35], s[30:31]
	s_add_u32 s38, s24, s26
	s_add_u32 s38, s38, 4
	s_sub_u32 s2, s38, 0x10400
	s_cmp_ge_u32 s38, 0x10400
	s_cselect_b32 s3, s2, s38
	s_cselect_b32 s6, 1, 0
	s_cmp_ge_u32 s3, 0x8200
	s_cselect_b32 s7, 1, 0
	s_mul_i32 s2, s7, 0x8200
	s_sub_u32 s3, s3, s2
	s_lshr_b32 s34, s3, 9
	s_and_b32 s3, s3, 0x1ff
	s_cmp_eq_u32 s6, 1
	s_cselect_b32 s35, 7, 5
	s_cselect_b32 s45, 63, 15
	s_lshr_b32 s2, s3, s35
	s_lshl_b32 s2, s2, 1
	s_and_b32 s39, s3, 1
	s_or_b32 s39, s2, s39
	s_lshr_b32 s2, s3, 1
	s_and_b32 s40, s2, s45
	s_cmp_eq_u32 s7, 1
	s_cselect_b64 s[44:45], s[14:15], s[12:13]
	s_cselect_b64 s[2:3], s[20:21], s[18:19]
	s_cmp_eq_u32 s6, 1
	s_cselect_b64 s[44:45], s[16:17], s[44:45]
	s_cselect_b64 s[2:3], s[22:23], s[2:3]
	s_cselect_b32 s35, 19, 17
	s_cselect_b32 s36, 2, 0
	s_cmp_lt_u32 s34, 64
	s_cselect_b64 s[28:29], s[44:45], s[2:3]
	s_cselect_b32 s34, s34, 0
	s_lshl_b32 s34, s34, 22
	s_lshl_b32 s2, s39, s35
	s_add_u32 s34, s34, s2
	s_lshl_b32 s2, s40, 7
	s_add_u32 s34, s34, s2
	s_add_u32 s28, s28, s34
	s_addc_u32 s29, s29, 0
	v_lshl_add_u32 v13, v2, s36, v10
	v_lshl_add_u32 v14, v3, s36, v10
	v_lshl_add_u32 v15, v4, s36, v10
	v_lshl_add_u32 v16, v5, s36, v10
	v_lshl_add_u32 v17, v6, s36, v10
	v_lshl_add_u32 v18, v7, s36, v10
	v_lshl_add_u32 v19, v8, s36, v10
	v_lshl_add_u32 v20, v9, s36, v10
	global_load_dwordx4 v[48:51], v13, s[28:29]
	global_load_dwordx4 v[52:55], v14, s[28:29]
	global_load_dwordx4 v[56:59], v15, s[28:29]
	global_load_dwordx4 v[60:63], v16, s[28:29]
	global_load_dwordx4 v[64:67], v17, s[28:29]
	global_load_dwordx4 v[68:71], v18, s[28:29]
	global_load_dwordx4 v[72:75], v19, s[28:29]
	global_load_dwordx4 v[76:79], v20, s[28:29]
	s_waitcnt vmcnt(36)
	s_add_u32 s38, s24, s26
	s_add_u32 s38, s38, 1
	s_sub_u32 s2, s38, 0x10400
	s_cmp_ge_u32 s38, 0x10400
	s_cselect_b32 s3, s2, s38
	s_cselect_b32 s6, 1, 0
	s_cmp_ge_u32 s3, 0x8200
	s_cselect_b32 s7, 1, 0
	s_mul_i32 s2, s7, 0x8200
	s_sub_u32 s3, s3, s2
	s_lshr_b32 s34, s3, 9
	s_and_b32 s3, s3, 0x1ff
	s_cmp_eq_u32 s6, 1
	s_cselect_b32 s35, 7, 5
	s_cselect_b32 s45, 63, 15
	s_lshr_b32 s2, s3, s35
	s_lshl_b32 s2, s2, 1
	s_and_b32 s39, s3, 1
	s_or_b32 s39, s2, s39
	s_lshr_b32 s2, s3, 1
	s_and_b32 s40, s2, s45
	s_cmp_eq_u32 s6, 1
	s_cselect_b32 s35, 20, 21
	s_cselect_b32 s36, 0, 2
	s_cselect_b32 s41, 0, 0x800000
	s_cselect_b32 s2, 0x10400000, 0
	s_lshl_b32 s37, 0x200, s36
	s_add_u32 s41, s41, 0x42000000
	s_add_u32 s2, s2, 0x2400000
	s_lshl_b32 s34, s34, s35
	s_add_u32 s34, s34, s2
	s_lshr_b32 s2, s40, 2
	s_lshl_b32 s2, s2, 8
	s_lshl_b32 s3, s7, 7
	s_add_u32 s2, s2, s3
	s_and_b32 s3, s40, 3
	s_lshl_b32 s3, s3, 5
	s_add_u32 s2, s2, s3
	s_lshl_b32 s2, s2, 11
	s_lshl_b32 s3, s40, 14
	s_cmp_eq_u32 s6, 1
	s_cselect_b32 s2, s3, s2
	s_add_u32 s34, s34, s2
	s_lshl_b32 s2, s39, 6
	s_add_u32 s34, s34, s2
	s_add_u32 s30, s10, s34
	s_addc_u32 s31, s11, 0
	v_lshl_add_u32 v21, v11, s36, v12
	s_lshl_b32 s2, s37, 1
	s_add_u32 s3, s2, s37
	v_add_u32_e32 v22, s37, v21
	v_add_u32_e32 v23, s2, v21
	v_add_u32_e32 v24, s3, v21
	v_mul_f32_e32 v36, s41, v80
	v_mul_f32_e32 v37, s41, v84
	v_mul_f32_e32 v38, s41, v88
	v_mul_f32_e32 v39, s41, v92
	v_mul_f32_e32 v40, s41, v96
	v_mul_f32_e32 v41, s41, v100
	v_mul_f32_e32 v42, s41, v104
	v_mul_f32_e32 v43, s41, v108
	v_med3_f32 v36, v36, s27, v1
	v_med3_f32 v37, v37, s27, v1
	v_med3_f32 v38, v38, s27, v1
	v_med3_f32 v39, v39, s27, v1
	v_med3_f32 v40, v40, s27, v1
	v_med3_f32 v41, v41, s27, v1
	v_med3_f32 v42, v42, s27, v1
	v_med3_f32 v43, v43, s27, v1
	v_cvt_pk_fp8_f32 v28, v36, v37
	v_cvt_pk_fp8_f32 v29, v40, v41
	v_cvt_pk_fp8_f32 v28, v38, v39 op_sel:[0,0,1]
	v_cvt_pk_fp8_f32 v29, v42, v43 op_sel:[0,0,1]
	s_nop 0
	global_store_dwordx2 v21, v[28:29], s[30:31]
	v_mul_f32_e32 v36, s41, v81
	v_mul_f32_e32 v37, s41, v85
	v_mul_f32_e32 v38, s41, v89
	v_mul_f32_e32 v39, s41, v93
	v_mul_f32_e32 v40, s41, v97
	v_mul_f32_e32 v41, s41, v101
	v_mul_f32_e32 v42, s41, v105
	v_mul_f32_e32 v43, s41, v109
	v_med3_f32 v36, v36, s27, v1
	v_med3_f32 v37, v37, s27, v1
	v_med3_f32 v38, v38, s27, v1
	v_med3_f32 v39, v39, s27, v1
	v_med3_f32 v40, v40, s27, v1
	v_med3_f32 v41, v41, s27, v1
	v_med3_f32 v42, v42, s27, v1
	v_med3_f32 v43, v43, s27, v1
	v_cvt_pk_fp8_f32 v30, v36, v37
	v_cvt_pk_fp8_f32 v31, v40, v41
	v_cvt_pk_fp8_f32 v30, v38, v39 op_sel:[0,0,1]
	v_cvt_pk_fp8_f32 v31, v42, v43 op_sel:[0,0,1]
	s_nop 0
	global_store_dwordx2 v22, v[30:31], s[30:31]
	v_mul_f32_e32 v36, s41, v82
	v_mul_f32_e32 v37, s41, v86
	v_mul_f32_e32 v38, s41, v90
	v_mul_f32_e32 v39, s41, v94
	v_mul_f32_e32 v40, s41, v98
	v_mul_f32_e32 v41, s41, v102
	v_mul_f32_e32 v42, s41, v106
	v_mul_f32_e32 v43, s41, v110
	v_med3_f32 v36, v36, s27, v1
	v_med3_f32 v37, v37, s27, v1
	v_med3_f32 v38, v38, s27, v1
	v_med3_f32 v39, v39, s27, v1
	v_med3_f32 v40, v40, s27, v1
	v_med3_f32 v41, v41, s27, v1
	v_med3_f32 v42, v42, s27, v1
	v_med3_f32 v43, v43, s27, v1
	v_cvt_pk_fp8_f32 v32, v36, v37
	v_cvt_pk_fp8_f32 v33, v40, v41
	v_cvt_pk_fp8_f32 v32, v38, v39 op_sel:[0,0,1]
	v_cvt_pk_fp8_f32 v33, v42, v43 op_sel:[0,0,1]
	s_nop 0
	global_store_dwordx2 v23, v[32:33], s[30:31]
	v_mul_f32_e32 v36, s41, v83
	v_mul_f32_e32 v37, s41, v87
	v_mul_f32_e32 v38, s41, v91
	v_mul_f32_e32 v39, s41, v95
	v_mul_f32_e32 v40, s41, v99
	v_mul_f32_e32 v41, s41, v103
	v_mul_f32_e32 v42, s41, v107
	v_mul_f32_e32 v43, s41, v111
	v_med3_f32 v36, v36, s27, v1
	v_med3_f32 v37, v37, s27, v1
	v_med3_f32 v38, v38, s27, v1
	v_med3_f32 v39, v39, s27, v1
	v_med3_f32 v40, v40, s27, v1
	v_med3_f32 v41, v41, s27, v1
	v_med3_f32 v42, v42, s27, v1
	v_med3_f32 v43, v43, s27, v1
	v_cvt_pk_fp8_f32 v34, v36, v37
	v_cvt_pk_fp8_f32 v35, v40, v41
	v_cvt_pk_fp8_f32 v34, v38, v39 op_sel:[0,0,1]
	v_cvt_pk_fp8_f32 v35, v42, v43 op_sel:[0,0,1]
	s_nop 0
	global_store_dwordx2 v24, v[34:35], s[30:31]
	s_add_u32 s38, s24, s26
	s_add_u32 s38, s38, 5
	s_sub_u32 s2, s38, 0x10400
	s_cmp_ge_u32 s38, 0x10400
	s_cselect_b32 s3, s2, s38
	s_cselect_b32 s6, 1, 0
	s_cmp_ge_u32 s3, 0x8200
	s_cselect_b32 s7, 1, 0
	s_mul_i32 s2, s7, 0x8200
	s_sub_u32 s3, s3, s2
	s_lshr_b32 s34, s3, 9
	s_and_b32 s3, s3, 0x1ff
	s_cmp_eq_u32 s6, 1
	s_cselect_b32 s35, 7, 5
	s_cselect_b32 s45, 63, 15
	s_lshr_b32 s2, s3, s35
	s_lshl_b32 s2, s2, 1
	s_and_b32 s39, s3, 1
	s_or_b32 s39, s2, s39
	s_lshr_b32 s2, s3, 1
	s_and_b32 s40, s2, s45
	s_cmp_eq_u32 s7, 1
	s_cselect_b64 s[44:45], s[14:15], s[12:13]
	s_cselect_b64 s[2:3], s[20:21], s[18:19]
	s_cmp_eq_u32 s6, 1
	s_cselect_b64 s[44:45], s[16:17], s[44:45]
	s_cselect_b64 s[2:3], s[22:23], s[2:3]
	s_cselect_b32 s35, 19, 17
	s_cselect_b32 s36, 2, 0
	s_cmp_lt_u32 s34, 64
	s_cselect_b64 s[42:43], s[44:45], s[2:3]
	s_cselect_b32 s34, s34, 0
	s_lshl_b32 s34, s34, 22
	s_lshl_b32 s2, s39, s35
	s_add_u32 s34, s34, s2
	s_lshl_b32 s2, s40, 7
	s_add_u32 s34, s34, s2
	s_add_u32 s42, s42, s34
	s_addc_u32 s43, s43, 0
	v_lshl_add_u32 v13, v2, s36, v10
	v_lshl_add_u32 v14, v3, s36, v10
	v_lshl_add_u32 v15, v4, s36, v10
	v_lshl_add_u32 v16, v5, s36, v10
	v_lshl_add_u32 v17, v6, s36, v10
	v_lshl_add_u32 v18, v7, s36, v10
	v_lshl_add_u32 v19, v8, s36, v10
	v_lshl_add_u32 v20, v9, s36, v10
	global_load_dwordx4 v[80:83], v13, s[42:43]
	global_load_dwordx4 v[84:87], v14, s[42:43]
	global_load_dwordx4 v[88:91], v15, s[42:43]
	global_load_dwordx4 v[92:95], v16, s[42:43]
	global_load_dwordx4 v[96:99], v17, s[42:43]
	global_load_dwordx4 v[100:103], v18, s[42:43]
	global_load_dwordx4 v[104:107], v19, s[42:43]
	global_load_dwordx4 v[108:111], v20, s[42:43]
	s_waitcnt vmcnt(36)
	s_add_u32 s38, s24, s26
	s_add_u32 s38, s38, 2
	s_sub_u32 s2, s38, 0x10400
	s_cmp_ge_u32 s38, 0x10400
	s_cselect_b32 s3, s2, s38
	s_cselect_b32 s6, 1, 0
	s_cmp_ge_u32 s3, 0x8200
	s_cselect_b32 s7, 1, 0
	s_mul_i32 s2, s7, 0x8200
	s_sub_u32 s3, s3, s2
	s_lshr_b32 s34, s3, 9
	s_and_b32 s3, s3, 0x1ff
	s_cmp_eq_u32 s6, 1
	s_cselect_b32 s35, 7, 5
	s_cselect_b32 s45, 63, 15
	s_lshr_b32 s2, s3, s35
	s_lshl_b32 s2, s2, 1
	s_and_b32 s39, s3, 1
	s_or_b32 s39, s2, s39
	s_lshr_b32 s2, s3, 1
	s_and_b32 s40, s2, s45
	s_cmp_eq_u32 s6, 1
	s_cselect_b32 s35, 20, 21
	s_cselect_b32 s36, 0, 2
	s_cselect_b32 s41, 0, 0x800000
	s_cselect_b32 s2, 0x10400000, 0
	s_lshl_b32 s37, 0x200, s36
	s_add_u32 s41, s41, 0x42000000
	s_add_u32 s2, s2, 0x2400000
	s_lshl_b32 s34, s34, s35
	s_add_u32 s34, s34, s2
	s_lshr_b32 s2, s40, 2
	s_lshl_b32 s2, s2, 8
	s_lshl_b32 s3, s7, 7
	s_add_u32 s2, s2, s3
	s_and_b32 s3, s40, 3
	s_lshl_b32 s3, s3, 5
	s_add_u32 s2, s2, s3
	s_lshl_b32 s2, s2, 11
	s_lshl_b32 s3, s40, 14
	s_cmp_eq_u32 s6, 1
	s_cselect_b32 s2, s3, s2
	s_add_u32 s34, s34, s2
	s_lshl_b32 s2, s39, 6
	s_add_u32 s34, s34, s2
	s_add_u32 s30, s10, s34
	s_addc_u32 s31, s11, 0
	v_lshl_add_u32 v21, v11, s36, v12
	s_lshl_b32 s2, s37, 1
	s_add_u32 s3, s2, s37
	v_add_u32_e32 v22, s37, v21
	v_add_u32_e32 v23, s2, v21
	v_add_u32_e32 v24, s3, v21
	v_mul_f32_e32 v36, s41, v112
	v_mul_f32_e32 v37, s41, v116
	v_mul_f32_e32 v38, s41, v120
	v_mul_f32_e32 v39, s41, v124
	v_mul_f32_e32 v40, s41, v128
	v_mul_f32_e32 v41, s41, v132
	v_mul_f32_e32 v42, s41, v136
	v_mul_f32_e32 v43, s41, v140
	v_med3_f32 v36, v36, s27, v1
	v_med3_f32 v37, v37, s27, v1
	v_med3_f32 v38, v38, s27, v1
	v_med3_f32 v39, v39, s27, v1
	v_med3_f32 v40, v40, s27, v1
	v_med3_f32 v41, v41, s27, v1
	v_med3_f32 v42, v42, s27, v1
	v_med3_f32 v43, v43, s27, v1
	v_cvt_pk_fp8_f32 v28, v36, v37
	v_cvt_pk_fp8_f32 v29, v40, v41
	v_cvt_pk_fp8_f32 v28, v38, v39 op_sel:[0,0,1]
	v_cvt_pk_fp8_f32 v29, v42, v43 op_sel:[0,0,1]
	s_nop 0
	global_store_dwordx2 v21, v[28:29], s[30:31]
	v_mul_f32_e32 v36, s41, v113
	v_mul_f32_e32 v37, s41, v117
	v_mul_f32_e32 v38, s41, v121
	v_mul_f32_e32 v39, s41, v125
	v_mul_f32_e32 v40, s41, v129
	v_mul_f32_e32 v41, s41, v133
	v_mul_f32_e32 v42, s41, v137
	v_mul_f32_e32 v43, s41, v141
	v_med3_f32 v36, v36, s27, v1
	v_med3_f32 v37, v37, s27, v1
	v_med3_f32 v38, v38, s27, v1
	v_med3_f32 v39, v39, s27, v1
	v_med3_f32 v40, v40, s27, v1
	v_med3_f32 v41, v41, s27, v1
	v_med3_f32 v42, v42, s27, v1
	v_med3_f32 v43, v43, s27, v1
	v_cvt_pk_fp8_f32 v30, v36, v37
	v_cvt_pk_fp8_f32 v31, v40, v41
	v_cvt_pk_fp8_f32 v30, v38, v39 op_sel:[0,0,1]
	v_cvt_pk_fp8_f32 v31, v42, v43 op_sel:[0,0,1]
	s_nop 0
	global_store_dwordx2 v22, v[30:31], s[30:31]
	v_mul_f32_e32 v36, s41, v114
	v_mul_f32_e32 v37, s41, v118
	v_mul_f32_e32 v38, s41, v122
	v_mul_f32_e32 v39, s41, v126
	v_mul_f32_e32 v40, s41, v130
	v_mul_f32_e32 v41, s41, v134
	v_mul_f32_e32 v42, s41, v138
	v_mul_f32_e32 v43, s41, v142
	v_med3_f32 v36, v36, s27, v1
	v_med3_f32 v37, v37, s27, v1
	v_med3_f32 v38, v38, s27, v1
	v_med3_f32 v39, v39, s27, v1
	v_med3_f32 v40, v40, s27, v1
	v_med3_f32 v41, v41, s27, v1
	v_med3_f32 v42, v42, s27, v1
	v_med3_f32 v43, v43, s27, v1
	v_cvt_pk_fp8_f32 v32, v36, v37
	v_cvt_pk_fp8_f32 v33, v40, v41
	v_cvt_pk_fp8_f32 v32, v38, v39 op_sel:[0,0,1]
	v_cvt_pk_fp8_f32 v33, v42, v43 op_sel:[0,0,1]
	s_nop 0
	global_store_dwordx2 v23, v[32:33], s[30:31]
	v_mul_f32_e32 v36, s41, v115
	v_mul_f32_e32 v37, s41, v119
	v_mul_f32_e32 v38, s41, v123
	v_mul_f32_e32 v39, s41, v127
	v_mul_f32_e32 v40, s41, v131
	v_mul_f32_e32 v41, s41, v135
	v_mul_f32_e32 v42, s41, v139
	v_mul_f32_e32 v43, s41, v143
	v_med3_f32 v36, v36, s27, v1
	v_med3_f32 v37, v37, s27, v1
	v_med3_f32 v38, v38, s27, v1
	v_med3_f32 v39, v39, s27, v1
	v_med3_f32 v40, v40, s27, v1
	v_med3_f32 v41, v41, s27, v1
	v_med3_f32 v42, v42, s27, v1
	v_med3_f32 v43, v43, s27, v1
	v_cvt_pk_fp8_f32 v34, v36, v37
	v_cvt_pk_fp8_f32 v35, v40, v41
	v_cvt_pk_fp8_f32 v34, v38, v39 op_sel:[0,0,1]
	v_cvt_pk_fp8_f32 v35, v42, v43 op_sel:[0,0,1]
	s_nop 0
	global_store_dwordx2 v24, v[34:35], s[30:31]
	s_add_u32 s38, s24, s26
	s_add_u32 s38, s38, 6
	s_sub_u32 s2, s38, 0x10400
	s_cmp_ge_u32 s38, 0x10400
	s_cselect_b32 s3, s2, s38
	s_cselect_b32 s6, 1, 0
	s_cmp_ge_u32 s3, 0x8200
	s_cselect_b32 s7, 1, 0
	s_mul_i32 s2, s7, 0x8200
	s_sub_u32 s3, s3, s2
	s_lshr_b32 s34, s3, 9
	s_and_b32 s3, s3, 0x1ff
	s_cmp_eq_u32 s6, 1
	s_cselect_b32 s35, 7, 5
	s_cselect_b32 s45, 63, 15
	s_lshr_b32 s2, s3, s35
	s_lshl_b32 s2, s2, 1
	s_and_b32 s39, s3, 1
	s_or_b32 s39, s2, s39
	s_lshr_b32 s2, s3, 1
	s_and_b32 s40, s2, s45
	s_cmp_eq_u32 s7, 1
	s_cselect_b64 s[44:45], s[14:15], s[12:13]
	s_cselect_b64 s[2:3], s[20:21], s[18:19]
	s_cmp_eq_u32 s6, 1
	s_cselect_b64 s[44:45], s[16:17], s[44:45]
	s_cselect_b64 s[2:3], s[22:23], s[2:3]
	s_cselect_b32 s35, 19, 17
	s_cselect_b32 s36, 2, 0
	s_cmp_lt_u32 s34, 64
	s_cselect_b64 s[28:29], s[44:45], s[2:3]
	s_cselect_b32 s34, s34, 0
	s_lshl_b32 s34, s34, 22
	s_lshl_b32 s2, s39, s35
	s_add_u32 s34, s34, s2
	s_lshl_b32 s2, s40, 7
	s_add_u32 s34, s34, s2
	s_add_u32 s28, s28, s34
	s_addc_u32 s29, s29, 0
	v_lshl_add_u32 v13, v2, s36, v10
	v_lshl_add_u32 v14, v3, s36, v10
	v_lshl_add_u32 v15, v4, s36, v10
	v_lshl_add_u32 v16, v5, s36, v10
	v_lshl_add_u32 v17, v6, s36, v10
	v_lshl_add_u32 v18, v7, s36, v10
	v_lshl_add_u32 v19, v8, s36, v10
	v_lshl_add_u32 v20, v9, s36, v10
	global_load_dwordx4 v[112:115], v13, s[28:29]
	global_load_dwordx4 v[116:119], v14, s[28:29]
	global_load_dwordx4 v[120:123], v15, s[28:29]
	global_load_dwordx4 v[124:127], v16, s[28:29]
	global_load_dwordx4 v[128:131], v17, s[28:29]
	global_load_dwordx4 v[132:135], v18, s[28:29]
	global_load_dwordx4 v[136:139], v19, s[28:29]
	global_load_dwordx4 v[140:143], v20, s[28:29]
	s_waitcnt vmcnt(36)
	s_add_u32 s38, s24, s26
	s_add_u32 s38, s38, 3
	s_sub_u32 s2, s38, 0x10400
	s_cmp_ge_u32 s38, 0x10400
	s_cselect_b32 s3, s2, s38
	s_cselect_b32 s6, 1, 0
	s_cmp_ge_u32 s3, 0x8200
	s_cselect_b32 s7, 1, 0
	s_mul_i32 s2, s7, 0x8200
	s_sub_u32 s3, s3, s2
	s_lshr_b32 s34, s3, 9
	s_and_b32 s3, s3, 0x1ff
	s_cmp_eq_u32 s6, 1
	s_cselect_b32 s35, 7, 5
	s_cselect_b32 s45, 63, 15
	s_lshr_b32 s2, s3, s35
	s_lshl_b32 s2, s2, 1
	s_and_b32 s39, s3, 1
	s_or_b32 s39, s2, s39
	s_lshr_b32 s2, s3, 1
	s_and_b32 s40, s2, s45
	s_cmp_eq_u32 s6, 1
	s_cselect_b32 s35, 20, 21
	s_cselect_b32 s36, 0, 2
	s_cselect_b32 s41, 0, 0x800000
	s_cselect_b32 s2, 0x10400000, 0
	s_lshl_b32 s37, 0x200, s36
	s_add_u32 s41, s41, 0x42000000
	s_add_u32 s2, s2, 0x2400000
	s_lshl_b32 s34, s34, s35
	s_add_u32 s34, s34, s2
	s_lshr_b32 s2, s40, 2
	s_lshl_b32 s2, s2, 8
	s_lshl_b32 s3, s7, 7
	s_add_u32 s2, s2, s3
	s_and_b32 s3, s40, 3
	s_lshl_b32 s3, s3, 5
	s_add_u32 s2, s2, s3
	s_lshl_b32 s2, s2, 11
	s_lshl_b32 s3, s40, 14
	s_cmp_eq_u32 s6, 1
	s_cselect_b32 s2, s3, s2
	s_add_u32 s34, s34, s2
	s_lshl_b32 s2, s39, 6
	s_add_u32 s34, s34, s2
	s_add_u32 s30, s10, s34
	s_addc_u32 s31, s11, 0
	v_lshl_add_u32 v21, v11, s36, v12
	s_lshl_b32 s2, s37, 1
	s_add_u32 s3, s2, s37
	v_add_u32_e32 v22, s37, v21
	v_add_u32_e32 v23, s2, v21
	v_add_u32_e32 v24, s3, v21
	v_mul_f32_e32 v36, s41, v144
	v_mul_f32_e32 v37, s41, v148
	v_mul_f32_e32 v38, s41, v152
	v_mul_f32_e32 v39, s41, v156
	v_mul_f32_e32 v40, s41, v160
	v_mul_f32_e32 v41, s41, v164
	v_mul_f32_e32 v42, s41, v168
	v_mul_f32_e32 v43, s41, v172
	v_med3_f32 v36, v36, s27, v1
	v_med3_f32 v37, v37, s27, v1
	v_med3_f32 v38, v38, s27, v1
	v_med3_f32 v39, v39, s27, v1
	v_med3_f32 v40, v40, s27, v1
	v_med3_f32 v41, v41, s27, v1
	v_med3_f32 v42, v42, s27, v1
	v_med3_f32 v43, v43, s27, v1
	v_cvt_pk_fp8_f32 v28, v36, v37
	v_cvt_pk_fp8_f32 v29, v40, v41
	v_cvt_pk_fp8_f32 v28, v38, v39 op_sel:[0,0,1]
	v_cvt_pk_fp8_f32 v29, v42, v43 op_sel:[0,0,1]
	s_nop 0
	global_store_dwordx2 v21, v[28:29], s[30:31]
	v_mul_f32_e32 v36, s41, v145
	v_mul_f32_e32 v37, s41, v149
	v_mul_f32_e32 v38, s41, v153
	v_mul_f32_e32 v39, s41, v157
	v_mul_f32_e32 v40, s41, v161
	v_mul_f32_e32 v41, s41, v165
	v_mul_f32_e32 v42, s41, v169
	v_mul_f32_e32 v43, s41, v173
	v_med3_f32 v36, v36, s27, v1
	v_med3_f32 v37, v37, s27, v1
	v_med3_f32 v38, v38, s27, v1
	v_med3_f32 v39, v39, s27, v1
	v_med3_f32 v40, v40, s27, v1
	v_med3_f32 v41, v41, s27, v1
	v_med3_f32 v42, v42, s27, v1
	v_med3_f32 v43, v43, s27, v1
	v_cvt_pk_fp8_f32 v30, v36, v37
	v_cvt_pk_fp8_f32 v31, v40, v41
	v_cvt_pk_fp8_f32 v30, v38, v39 op_sel:[0,0,1]
	v_cvt_pk_fp8_f32 v31, v42, v43 op_sel:[0,0,1]
	s_nop 0
	global_store_dwordx2 v22, v[30:31], s[30:31]
	v_mul_f32_e32 v36, s41, v146
	v_mul_f32_e32 v37, s41, v150
	v_mul_f32_e32 v38, s41, v154
	v_mul_f32_e32 v39, s41, v158
	v_mul_f32_e32 v40, s41, v162
	v_mul_f32_e32 v41, s41, v166
	v_mul_f32_e32 v42, s41, v170
	v_mul_f32_e32 v43, s41, v174
	v_med3_f32 v36, v36, s27, v1
	v_med3_f32 v37, v37, s27, v1
	v_med3_f32 v38, v38, s27, v1
	v_med3_f32 v39, v39, s27, v1
	v_med3_f32 v40, v40, s27, v1
	v_med3_f32 v41, v41, s27, v1
	v_med3_f32 v42, v42, s27, v1
	v_med3_f32 v43, v43, s27, v1
	v_cvt_pk_fp8_f32 v32, v36, v37
	v_cvt_pk_fp8_f32 v33, v40, v41
	v_cvt_pk_fp8_f32 v32, v38, v39 op_sel:[0,0,1]
	v_cvt_pk_fp8_f32 v33, v42, v43 op_sel:[0,0,1]
	s_nop 0
	global_store_dwordx2 v23, v[32:33], s[30:31]
	v_mul_f32_e32 v36, s41, v147
	v_mul_f32_e32 v37, s41, v151
	v_mul_f32_e32 v38, s41, v155
	v_mul_f32_e32 v39, s41, v159
	v_mul_f32_e32 v40, s41, v163
	v_mul_f32_e32 v41, s41, v167
	v_mul_f32_e32 v42, s41, v171
	v_mul_f32_e32 v43, s41, v175
	v_med3_f32 v36, v36, s27, v1
	v_med3_f32 v37, v37, s27, v1
	v_med3_f32 v38, v38, s27, v1
	v_med3_f32 v39, v39, s27, v1
	v_med3_f32 v40, v40, s27, v1
	v_med3_f32 v41, v41, s27, v1
	v_med3_f32 v42, v42, s27, v1
	v_med3_f32 v43, v43, s27, v1
	v_cvt_pk_fp8_f32 v34, v36, v37
	v_cvt_pk_fp8_f32 v35, v40, v41
	v_cvt_pk_fp8_f32 v34, v38, v39 op_sel:[0,0,1]
	v_cvt_pk_fp8_f32 v35, v42, v43 op_sel:[0,0,1]
	s_nop 0
	global_store_dwordx2 v24, v[34:35], s[30:31]
	s_add_u32 s38, s24, s26
	s_add_u32 s38, s38, 7
	s_sub_u32 s2, s38, 0x10400
	s_cmp_ge_u32 s38, 0x10400
	s_cselect_b32 s3, s2, s38
	s_cselect_b32 s6, 1, 0
	s_cmp_ge_u32 s3, 0x8200
	s_cselect_b32 s7, 1, 0
	s_mul_i32 s2, s7, 0x8200
	s_sub_u32 s3, s3, s2
	s_lshr_b32 s34, s3, 9
	s_and_b32 s3, s3, 0x1ff
	s_cmp_eq_u32 s6, 1
	s_cselect_b32 s35, 7, 5
	s_cselect_b32 s45, 63, 15
	s_lshr_b32 s2, s3, s35
	s_lshl_b32 s2, s2, 1
	s_and_b32 s39, s3, 1
	s_or_b32 s39, s2, s39
	s_lshr_b32 s2, s3, 1
	s_and_b32 s40, s2, s45
	s_cmp_eq_u32 s7, 1
	s_cselect_b64 s[44:45], s[14:15], s[12:13]
	s_cselect_b64 s[2:3], s[20:21], s[18:19]
	s_cmp_eq_u32 s6, 1
	s_cselect_b64 s[44:45], s[16:17], s[44:45]
	s_cselect_b64 s[2:3], s[22:23], s[2:3]
	s_cselect_b32 s35, 19, 17
	s_cselect_b32 s36, 2, 0
	s_cmp_lt_u32 s34, 64
	s_cselect_b64 s[42:43], s[44:45], s[2:3]
	s_cselect_b32 s34, s34, 0
	s_lshl_b32 s34, s34, 22
	s_lshl_b32 s2, s39, s35
	s_add_u32 s34, s34, s2
	s_lshl_b32 s2, s40, 7
	s_add_u32 s34, s34, s2
	s_add_u32 s42, s42, s34
	s_addc_u32 s43, s43, 0
	v_lshl_add_u32 v13, v2, s36, v10
	v_lshl_add_u32 v14, v3, s36, v10
	v_lshl_add_u32 v15, v4, s36, v10
	v_lshl_add_u32 v16, v5, s36, v10
	v_lshl_add_u32 v17, v6, s36, v10
	v_lshl_add_u32 v18, v7, s36, v10
	v_lshl_add_u32 v19, v8, s36, v10
	v_lshl_add_u32 v20, v9, s36, v10
	global_load_dwordx4 v[144:147], v13, s[42:43]
	global_load_dwordx4 v[148:151], v14, s[42:43]
	global_load_dwordx4 v[152:155], v15, s[42:43]
	global_load_dwordx4 v[156:159], v16, s[42:43]
	global_load_dwordx4 v[160:163], v17, s[42:43]
	global_load_dwordx4 v[164:167], v18, s[42:43]
	global_load_dwordx4 v[168:171], v19, s[42:43]
	global_load_dwordx4 v[172:175], v20, s[42:43]
	s_add_u32 s26, s26, 4
	s_branch .Lcv_steady
.Lcv_drain:
	s_waitcnt vmcnt(0)
	s_add_u32 s38, s24, s26
	s_sub_u32 s2, s38, 0x10400
	s_cmp_ge_u32 s38, 0x10400
	s_cselect_b32 s3, s2, s38
	s_cselect_b32 s6, 1, 0
	s_cmp_ge_u32 s3, 0x8200
	s_cselect_b32 s7, 1, 0
	s_mul_i32 s2, s7, 0x8200
	s_sub_u32 s3, s3, s2
	s_lshr_b32 s34, s3, 9
	s_and_b32 s3, s3, 0x1ff
	s_cmp_eq_u32 s6, 1
	s_cselect_b32 s35, 7, 5
	s_cselect_b32 s45, 63, 15
	s_lshr_b32 s2, s3, s35
	s_lshl_b32 s2, s2, 1
	s_and_b32 s39, s3, 1
	s_or_b32 s39, s2, s39
	s_lshr_b32 s2, s3, 1
	s_and_b32 s40, s2, s45
	s_cmp_eq_u32 s6, 1
	s_cselect_b32 s35, 20, 21
	s_cselect_b32 s36, 0, 2
	s_cselect_b32 s41, 0, 0x800000
	s_cselect_b32 s2, 0x10400000, 0
	s_lshl_b32 s37, 0x200, s36
	s_add_u32 s41, s41, 0x42000000
	s_add_u32 s2, s2, 0x2400000
	s_lshl_b32 s34, s34, s35
	s_add_u32 s34, s34, s2
	s_lshr_b32 s2, s40, 2
	s_lshl_b32 s2, s2, 8
	s_lshl_b32 s3, s7, 7
	s_add_u32 s2, s2, s3
	s_and_b32 s3, s40, 3
	s_lshl_b32 s3, s3, 5
	s_add_u32 s2, s2, s3
	s_lshl_b32 s2, s2, 11
	s_lshl_b32 s3, s40, 14
	s_cmp_eq_u32 s6, 1
	s_cselect_b32 s2, s3, s2
	s_add_u32 s34, s34, s2
	s_lshl_b32 s2, s39, 6
	s_add_u32 s34, s34, s2
	s_add_u32 s30, s10, s34
	s_addc_u32 s31, s11, 0
	v_lshl_add_u32 v21, v11, s36, v12
	s_lshl_b32 s2, s37, 1
	s_add_u32 s3, s2, s37
	v_add_u32_e32 v22, s37, v21
	v_add_u32_e32 v23, s2, v21
	v_add_u32_e32 v24, s3, v21
	v_mul_f32_e32 v36, s41, v48
	v_mul_f32_e32 v37, s41, v52
	v_mul_f32_e32 v38, s41, v56
	v_mul_f32_e32 v39, s41, v60
	v_mul_f32_e32 v40, s41, v64
	v_mul_f32_e32 v41, s41, v68
	v_mul_f32_e32 v42, s41, v72
	v_mul_f32_e32 v43, s41, v76
	v_med3_f32 v36, v36, s27, v1
	v_med3_f32 v37, v37, s27, v1
	v_med3_f32 v38, v38, s27, v1
	v_med3_f32 v39, v39, s27, v1
	v_med3_f32 v40, v40, s27, v1
	v_med3_f32 v41, v41, s27, v1
	v_med3_f32 v42, v42, s27, v1
	v_med3_f32 v43, v43, s27, v1
	v_cvt_pk_fp8_f32 v28, v36, v37
	v_cvt_pk_fp8_f32 v29, v40, v41
	v_cvt_pk_fp8_f32 v28, v38, v39 op_sel:[0,0,1]
	v_cvt_pk_fp8_f32 v29, v42, v43 op_sel:[0,0,1]
	s_nop 0
	global_store_dwordx2 v21, v[28:29], s[30:31]
	v_mul_f32_e32 v36, s41, v49
	v_mul_f32_e32 v37, s41, v53
	v_mul_f32_e32 v38, s41, v57
	v_mul_f32_e32 v39, s41, v61
	v_mul_f32_e32 v40, s41, v65
	v_mul_f32_e32 v41, s41, v69
	v_mul_f32_e32 v42, s41, v73
	v_mul_f32_e32 v43, s41, v77
	v_med3_f32 v36, v36, s27, v1
	v_med3_f32 v37, v37, s27, v1
	v_med3_f32 v38, v38, s27, v1
	v_med3_f32 v39, v39, s27, v1
	v_med3_f32 v40, v40, s27, v1
	v_med3_f32 v41, v41, s27, v1
	v_med3_f32 v42, v42, s27, v1
	v_med3_f32 v43, v43, s27, v1
	v_cvt_pk_fp8_f32 v30, v36, v37
	v_cvt_pk_fp8_f32 v31, v40, v41
	v_cvt_pk_fp8_f32 v30, v38, v39 op_sel:[0,0,1]
	v_cvt_pk_fp8_f32 v31, v42, v43 op_sel:[0,0,1]
	s_nop 0
	global_store_dwordx2 v22, v[30:31], s[30:31]
	v_mul_f32_e32 v36, s41, v50
	v_mul_f32_e32 v37, s41, v54
	v_mul_f32_e32 v38, s41, v58
	v_mul_f32_e32 v39, s41, v62
	v_mul_f32_e32 v40, s41, v66
	v_mul_f32_e32 v41, s41, v70
	v_mul_f32_e32 v42, s41, v74
	v_mul_f32_e32 v43, s41, v78
	v_med3_f32 v36, v36, s27, v1
	v_med3_f32 v37, v37, s27, v1
	v_med3_f32 v38, v38, s27, v1
	v_med3_f32 v39, v39, s27, v1
	v_med3_f32 v40, v40, s27, v1
	v_med3_f32 v41, v41, s27, v1
	v_med3_f32 v42, v42, s27, v1
	v_med3_f32 v43, v43, s27, v1
	v_cvt_pk_fp8_f32 v32, v36, v37
	v_cvt_pk_fp8_f32 v33, v40, v41
	v_cvt_pk_fp8_f32 v32, v38, v39 op_sel:[0,0,1]
	v_cvt_pk_fp8_f32 v33, v42, v43 op_sel:[0,0,1]
	s_nop 0
	global_store_dwordx2 v23, v[32:33], s[30:31]
	v_mul_f32_e32 v36, s41, v51
	v_mul_f32_e32 v37, s41, v55
	v_mul_f32_e32 v38, s41, v59
	v_mul_f32_e32 v39, s41, v63
	v_mul_f32_e32 v40, s41, v67
	v_mul_f32_e32 v41, s41, v71
	v_mul_f32_e32 v42, s41, v75
	v_mul_f32_e32 v43, s41, v79
	v_med3_f32 v36, v36, s27, v1
	v_med3_f32 v37, v37, s27, v1
	v_med3_f32 v38, v38, s27, v1
	v_med3_f32 v39, v39, s27, v1
	v_med3_f32 v40, v40, s27, v1
	v_med3_f32 v41, v41, s27, v1
	v_med3_f32 v42, v42, s27, v1
	v_med3_f32 v43, v43, s27, v1
	v_cvt_pk_fp8_f32 v34, v36, v37
	v_cvt_pk_fp8_f32 v35, v40, v41
	v_cvt_pk_fp8_f32 v34, v38, v39 op_sel:[0,0,1]
	v_cvt_pk_fp8_f32 v35, v42, v43 op_sel:[0,0,1]
	s_nop 0
	global_store_dwordx2 v24, v[34:35], s[30:31]
	s_add_u32 s38, s24, s26
	s_add_u32 s38, s38, 1
	s_sub_u32 s2, s38, 0x10400
	s_cmp_ge_u32 s38, 0x10400
	s_cselect_b32 s3, s2, s38
	s_cselect_b32 s6, 1, 0
	s_cmp_ge_u32 s3, 0x8200
	s_cselect_b32 s7, 1, 0
	s_mul_i32 s2, s7, 0x8200
	s_sub_u32 s3, s3, s2
	s_lshr_b32 s34, s3, 9
	s_and_b32 s3, s3, 0x1ff
	s_cmp_eq_u32 s6, 1
	s_cselect_b32 s35, 7, 5
	s_cselect_b32 s45, 63, 15
	s_lshr_b32 s2, s3, s35
	s_lshl_b32 s2, s2, 1
	s_and_b32 s39, s3, 1
	s_or_b32 s39, s2, s39
	s_lshr_b32 s2, s3, 1
	s_and_b32 s40, s2, s45
	s_cmp_eq_u32 s6, 1
	s_cselect_b32 s35, 20, 21
	s_cselect_b32 s36, 0, 2
	s_cselect_b32 s41, 0, 0x800000
	s_cselect_b32 s2, 0x10400000, 0
	s_lshl_b32 s37, 0x200, s36
	s_add_u32 s41, s41, 0x42000000
	s_add_u32 s2, s2, 0x2400000
	s_lshl_b32 s34, s34, s35
	s_add_u32 s34, s34, s2
	s_lshr_b32 s2, s40, 2
	s_lshl_b32 s2, s2, 8
	s_lshl_b32 s3, s7, 7
	s_add_u32 s2, s2, s3
	s_and_b32 s3, s40, 3
	s_lshl_b32 s3, s3, 5
	s_add_u32 s2, s2, s3
	s_lshl_b32 s2, s2, 11
	s_lshl_b32 s3, s40, 14
	s_cmp_eq_u32 s6, 1
	s_cselect_b32 s2, s3, s2
	s_add_u32 s34, s34, s2
	s_lshl_b32 s2, s39, 6
	s_add_u32 s34, s34, s2
	s_add_u32 s30, s10, s34
	s_addc_u32 s31, s11, 0
	v_lshl_add_u32 v21, v11, s36, v12
	s_lshl_b32 s2, s37, 1
	s_add_u32 s3, s2, s37
	v_add_u32_e32 v22, s37, v21
	v_add_u32_e32 v23, s2, v21
	v_add_u32_e32 v24, s3, v21
	v_mul_f32_e32 v36, s41, v80
	v_mul_f32_e32 v37, s41, v84
	v_mul_f32_e32 v38, s41, v88
	v_mul_f32_e32 v39, s41, v92
	v_mul_f32_e32 v40, s41, v96
	v_mul_f32_e32 v41, s41, v100
	v_mul_f32_e32 v42, s41, v104
	v_mul_f32_e32 v43, s41, v108
	v_med3_f32 v36, v36, s27, v1
	v_med3_f32 v37, v37, s27, v1
	v_med3_f32 v38, v38, s27, v1
	v_med3_f32 v39, v39, s27, v1
	v_med3_f32 v40, v40, s27, v1
	v_med3_f32 v41, v41, s27, v1
	v_med3_f32 v42, v42, s27, v1
	v_med3_f32 v43, v43, s27, v1
	v_cvt_pk_fp8_f32 v28, v36, v37
	v_cvt_pk_fp8_f32 v29, v40, v41
	v_cvt_pk_fp8_f32 v28, v38, v39 op_sel:[0,0,1]
	v_cvt_pk_fp8_f32 v29, v42, v43 op_sel:[0,0,1]
	s_nop 0
	global_store_dwordx2 v21, v[28:29], s[30:31]
	v_mul_f32_e32 v36, s41, v81
	v_mul_f32_e32 v37, s41, v85
	v_mul_f32_e32 v38, s41, v89
	v_mul_f32_e32 v39, s41, v93
	v_mul_f32_e32 v40, s41, v97
	v_mul_f32_e32 v41, s41, v101
	v_mul_f32_e32 v42, s41, v105
	v_mul_f32_e32 v43, s41, v109
	v_med3_f32 v36, v36, s27, v1
	v_med3_f32 v37, v37, s27, v1
	v_med3_f32 v38, v38, s27, v1
	v_med3_f32 v39, v39, s27, v1
	v_med3_f32 v40, v40, s27, v1
	v_med3_f32 v41, v41, s27, v1
	v_med3_f32 v42, v42, s27, v1
	v_med3_f32 v43, v43, s27, v1
	v_cvt_pk_fp8_f32 v30, v36, v37
	v_cvt_pk_fp8_f32 v31, v40, v41
	v_cvt_pk_fp8_f32 v30, v38, v39 op_sel:[0,0,1]
	v_cvt_pk_fp8_f32 v31, v42, v43 op_sel:[0,0,1]
	s_nop 0
	global_store_dwordx2 v22, v[30:31], s[30:31]
	v_mul_f32_e32 v36, s41, v82
	v_mul_f32_e32 v37, s41, v86
	v_mul_f32_e32 v38, s41, v90
	v_mul_f32_e32 v39, s41, v94
	v_mul_f32_e32 v40, s41, v98
	v_mul_f32_e32 v41, s41, v102
	v_mul_f32_e32 v42, s41, v106
	v_mul_f32_e32 v43, s41, v110
	v_med3_f32 v36, v36, s27, v1
	v_med3_f32 v37, v37, s27, v1
	v_med3_f32 v38, v38, s27, v1
	v_med3_f32 v39, v39, s27, v1
	v_med3_f32 v40, v40, s27, v1
	v_med3_f32 v41, v41, s27, v1
	v_med3_f32 v42, v42, s27, v1
	v_med3_f32 v43, v43, s27, v1
	v_cvt_pk_fp8_f32 v32, v36, v37
	v_cvt_pk_fp8_f32 v33, v40, v41
	v_cvt_pk_fp8_f32 v32, v38, v39 op_sel:[0,0,1]
	v_cvt_pk_fp8_f32 v33, v42, v43 op_sel:[0,0,1]
	s_nop 0
	global_store_dwordx2 v23, v[32:33], s[30:31]
	v_mul_f32_e32 v36, s41, v83
	v_mul_f32_e32 v37, s41, v87
	v_mul_f32_e32 v38, s41, v91
	v_mul_f32_e32 v39, s41, v95
	v_mul_f32_e32 v40, s41, v99
	v_mul_f32_e32 v41, s41, v103
	v_mul_f32_e32 v42, s41, v107
	v_mul_f32_e32 v43, s41, v111
	v_med3_f32 v36, v36, s27, v1
	v_med3_f32 v37, v37, s27, v1
	v_med3_f32 v38, v38, s27, v1
	v_med3_f32 v39, v39, s27, v1
	v_med3_f32 v40, v40, s27, v1
	v_med3_f32 v41, v41, s27, v1
	v_med3_f32 v42, v42, s27, v1
	v_med3_f32 v43, v43, s27, v1
	v_cvt_pk_fp8_f32 v34, v36, v37
	v_cvt_pk_fp8_f32 v35, v40, v41
	v_cvt_pk_fp8_f32 v34, v38, v39 op_sel:[0,0,1]
	v_cvt_pk_fp8_f32 v35, v42, v43 op_sel:[0,0,1]
	s_nop 0
	global_store_dwordx2 v24, v[34:35], s[30:31]
	s_add_u32 s38, s24, s26
	s_add_u32 s38, s38, 2
	s_sub_u32 s2, s38, 0x10400
	s_cmp_ge_u32 s38, 0x10400
	s_cselect_b32 s3, s2, s38
	s_cselect_b32 s6, 1, 0
	s_cmp_ge_u32 s3, 0x8200
	s_cselect_b32 s7, 1, 0
	s_mul_i32 s2, s7, 0x8200
	s_sub_u32 s3, s3, s2
	s_lshr_b32 s34, s3, 9
	s_and_b32 s3, s3, 0x1ff
	s_cmp_eq_u32 s6, 1
	s_cselect_b32 s35, 7, 5
	s_cselect_b32 s45, 63, 15
	s_lshr_b32 s2, s3, s35
	s_lshl_b32 s2, s2, 1
	s_and_b32 s39, s3, 1
	s_or_b32 s39, s2, s39
	s_lshr_b32 s2, s3, 1
	s_and_b32 s40, s2, s45
	s_cmp_eq_u32 s6, 1
	s_cselect_b32 s35, 20, 21
	s_cselect_b32 s36, 0, 2
	s_cselect_b32 s41, 0, 0x800000
	s_cselect_b32 s2, 0x10400000, 0
	s_lshl_b32 s37, 0x200, s36
	s_add_u32 s41, s41, 0x42000000
	s_add_u32 s2, s2, 0x2400000
	s_lshl_b32 s34, s34, s35
	s_add_u32 s34, s34, s2
	s_lshr_b32 s2, s40, 2
	s_lshl_b32 s2, s2, 8
	s_lshl_b32 s3, s7, 7
	s_add_u32 s2, s2, s3
	s_and_b32 s3, s40, 3
	s_lshl_b32 s3, s3, 5
	s_add_u32 s2, s2, s3
	s_lshl_b32 s2, s2, 11
	s_lshl_b32 s3, s40, 14
	s_cmp_eq_u32 s6, 1
	s_cselect_b32 s2, s3, s2
	s_add_u32 s34, s34, s2
	s_lshl_b32 s2, s39, 6
	s_add_u32 s34, s34, s2
	s_add_u32 s30, s10, s34
	s_addc_u32 s31, s11, 0
	v_lshl_add_u32 v21, v11, s36, v12
	s_lshl_b32 s2, s37, 1
	s_add_u32 s3, s2, s37
	v_add_u32_e32 v22, s37, v21
	v_add_u32_e32 v23, s2, v21
	v_add_u32_e32 v24, s3, v21
	v_mul_f32_e32 v36, s41, v112
	v_mul_f32_e32 v37, s41, v116
	v_mul_f32_e32 v38, s41, v120
	v_mul_f32_e32 v39, s41, v124
	v_mul_f32_e32 v40, s41, v128
	v_mul_f32_e32 v41, s41, v132
	v_mul_f32_e32 v42, s41, v136
	v_mul_f32_e32 v43, s41, v140
	v_med3_f32 v36, v36, s27, v1
	v_med3_f32 v37, v37, s27, v1
	v_med3_f32 v38, v38, s27, v1
	v_med3_f32 v39, v39, s27, v1
	v_med3_f32 v40, v40, s27, v1
	v_med3_f32 v41, v41, s27, v1
	v_med3_f32 v42, v42, s27, v1
	v_med3_f32 v43, v43, s27, v1
	v_cvt_pk_fp8_f32 v28, v36, v37
	v_cvt_pk_fp8_f32 v29, v40, v41
	v_cvt_pk_fp8_f32 v28, v38, v39 op_sel:[0,0,1]
	v_cvt_pk_fp8_f32 v29, v42, v43 op_sel:[0,0,1]
	s_nop 0
	global_store_dwordx2 v21, v[28:29], s[30:31]
	v_mul_f32_e32 v36, s41, v113
	v_mul_f32_e32 v37, s41, v117
	v_mul_f32_e32 v38, s41, v121
	v_mul_f32_e32 v39, s41, v125
	v_mul_f32_e32 v40, s41, v129
	v_mul_f32_e32 v41, s41, v133
	v_mul_f32_e32 v42, s41, v137
	v_mul_f32_e32 v43, s41, v141
	v_med3_f32 v36, v36, s27, v1
	v_med3_f32 v37, v37, s27, v1
	v_med3_f32 v38, v38, s27, v1
	v_med3_f32 v39, v39, s27, v1
	v_med3_f32 v40, v40, s27, v1
	v_med3_f32 v41, v41, s27, v1
	v_med3_f32 v42, v42, s27, v1
	v_med3_f32 v43, v43, s27, v1
	v_cvt_pk_fp8_f32 v30, v36, v37
	v_cvt_pk_fp8_f32 v31, v40, v41
	v_cvt_pk_fp8_f32 v30, v38, v39 op_sel:[0,0,1]
	v_cvt_pk_fp8_f32 v31, v42, v43 op_sel:[0,0,1]
	s_nop 0
	global_store_dwordx2 v22, v[30:31], s[30:31]
	v_mul_f32_e32 v36, s41, v114
	v_mul_f32_e32 v37, s41, v118
	v_mul_f32_e32 v38, s41, v122
	v_mul_f32_e32 v39, s41, v126
	v_mul_f32_e32 v40, s41, v130
	v_mul_f32_e32 v41, s41, v134
	v_mul_f32_e32 v42, s41, v138
	v_mul_f32_e32 v43, s41, v142
	v_med3_f32 v36, v36, s27, v1
	v_med3_f32 v37, v37, s27, v1
	v_med3_f32 v38, v38, s27, v1
	v_med3_f32 v39, v39, s27, v1
	v_med3_f32 v40, v40, s27, v1
	v_med3_f32 v41, v41, s27, v1
	v_med3_f32 v42, v42, s27, v1
	v_med3_f32 v43, v43, s27, v1
	v_cvt_pk_fp8_f32 v32, v36, v37
	v_cvt_pk_fp8_f32 v33, v40, v41
	v_cvt_pk_fp8_f32 v32, v38, v39 op_sel:[0,0,1]
	v_cvt_pk_fp8_f32 v33, v42, v43 op_sel:[0,0,1]
	s_nop 0
	global_store_dwordx2 v23, v[32:33], s[30:31]
	v_mul_f32_e32 v36, s41, v115
	v_mul_f32_e32 v37, s41, v119
	v_mul_f32_e32 v38, s41, v123
	v_mul_f32_e32 v39, s41, v127
	v_mul_f32_e32 v40, s41, v131
	v_mul_f32_e32 v41, s41, v135
	v_mul_f32_e32 v42, s41, v139
	v_mul_f32_e32 v43, s41, v143
	v_med3_f32 v36, v36, s27, v1
	v_med3_f32 v37, v37, s27, v1
	v_med3_f32 v38, v38, s27, v1
	v_med3_f32 v39, v39, s27, v1
	v_med3_f32 v40, v40, s27, v1
	v_med3_f32 v41, v41, s27, v1
	v_med3_f32 v42, v42, s27, v1
	v_med3_f32 v43, v43, s27, v1
	v_cvt_pk_fp8_f32 v34, v36, v37
	v_cvt_pk_fp8_f32 v35, v40, v41
	v_cvt_pk_fp8_f32 v34, v38, v39 op_sel:[0,0,1]
	v_cvt_pk_fp8_f32 v35, v42, v43 op_sel:[0,0,1]
	s_nop 0
	global_store_dwordx2 v24, v[34:35], s[30:31]
	s_add_u32 s38, s24, s26
	s_add_u32 s38, s38, 3
	s_sub_u32 s2, s38, 0x10400
	s_cmp_ge_u32 s38, 0x10400
	s_cselect_b32 s3, s2, s38
	s_cselect_b32 s6, 1, 0
	s_cmp_ge_u32 s3, 0x8200
	s_cselect_b32 s7, 1, 0
	s_mul_i32 s2, s7, 0x8200
	s_sub_u32 s3, s3, s2
	s_lshr_b32 s34, s3, 9
	s_and_b32 s3, s3, 0x1ff
	s_cmp_eq_u32 s6, 1
	s_cselect_b32 s35, 7, 5
	s_cselect_b32 s45, 63, 15
	s_lshr_b32 s2, s3, s35
	s_lshl_b32 s2, s2, 1
	s_and_b32 s39, s3, 1
	s_or_b32 s39, s2, s39
	s_lshr_b32 s2, s3, 1
	s_and_b32 s40, s2, s45
	s_cmp_eq_u32 s6, 1
	s_cselect_b32 s35, 20, 21
	s_cselect_b32 s36, 0, 2
	s_cselect_b32 s41, 0, 0x800000
	s_cselect_b32 s2, 0x10400000, 0
	s_lshl_b32 s37, 0x200, s36
	s_add_u32 s41, s41, 0x42000000
	s_add_u32 s2, s2, 0x2400000
	s_lshl_b32 s34, s34, s35
	s_add_u32 s34, s34, s2
	s_lshr_b32 s2, s40, 2
	s_lshl_b32 s2, s2, 8
	s_lshl_b32 s3, s7, 7
	s_add_u32 s2, s2, s3
	s_and_b32 s3, s40, 3
	s_lshl_b32 s3, s3, 5
	s_add_u32 s2, s2, s3
	s_lshl_b32 s2, s2, 11
	s_lshl_b32 s3, s40, 14
	s_cmp_eq_u32 s6, 1
	s_cselect_b32 s2, s3, s2
	s_add_u32 s34, s34, s2
	s_lshl_b32 s2, s39, 6
	s_add_u32 s34, s34, s2
	s_add_u32 s30, s10, s34
	s_addc_u32 s31, s11, 0
	v_lshl_add_u32 v21, v11, s36, v12
	s_lshl_b32 s2, s37, 1
	s_add_u32 s3, s2, s37
	v_add_u32_e32 v22, s37, v21
	v_add_u32_e32 v23, s2, v21
	v_add_u32_e32 v24, s3, v21
	v_mul_f32_e32 v36, s41, v144
	v_mul_f32_e32 v37, s41, v148
	v_mul_f32_e32 v38, s41, v152
	v_mul_f32_e32 v39, s41, v156
	v_mul_f32_e32 v40, s41, v160
	v_mul_f32_e32 v41, s41, v164
	v_mul_f32_e32 v42, s41, v168
	v_mul_f32_e32 v43, s41, v172
	v_med3_f32 v36, v36, s27, v1
	v_med3_f32 v37, v37, s27, v1
	v_med3_f32 v38, v38, s27, v1
	v_med3_f32 v39, v39, s27, v1
	v_med3_f32 v40, v40, s27, v1
	v_med3_f32 v41, v41, s27, v1
	v_med3_f32 v42, v42, s27, v1
	v_med3_f32 v43, v43, s27, v1
	v_cvt_pk_fp8_f32 v28, v36, v37
	v_cvt_pk_fp8_f32 v29, v40, v41
	v_cvt_pk_fp8_f32 v28, v38, v39 op_sel:[0,0,1]
	v_cvt_pk_fp8_f32 v29, v42, v43 op_sel:[0,0,1]
	s_nop 0
	global_store_dwordx2 v21, v[28:29], s[30:31]
	v_mul_f32_e32 v36, s41, v145
	v_mul_f32_e32 v37, s41, v149
	v_mul_f32_e32 v38, s41, v153
	v_mul_f32_e32 v39, s41, v157
	v_mul_f32_e32 v40, s41, v161
	v_mul_f32_e32 v41, s41, v165
	v_mul_f32_e32 v42, s41, v169
	v_mul_f32_e32 v43, s41, v173
	v_med3_f32 v36, v36, s27, v1
	v_med3_f32 v37, v37, s27, v1
	v_med3_f32 v38, v38, s27, v1
	v_med3_f32 v39, v39, s27, v1
	v_med3_f32 v40, v40, s27, v1
	v_med3_f32 v41, v41, s27, v1
	v_med3_f32 v42, v42, s27, v1
	v_med3_f32 v43, v43, s27, v1
	v_cvt_pk_fp8_f32 v30, v36, v37
	v_cvt_pk_fp8_f32 v31, v40, v41
	v_cvt_pk_fp8_f32 v30, v38, v39 op_sel:[0,0,1]
	v_cvt_pk_fp8_f32 v31, v42, v43 op_sel:[0,0,1]
	s_nop 0
	global_store_dwordx2 v22, v[30:31], s[30:31]
	v_mul_f32_e32 v36, s41, v146
	v_mul_f32_e32 v37, s41, v150
	v_mul_f32_e32 v38, s41, v154
	v_mul_f32_e32 v39, s41, v158
	v_mul_f32_e32 v40, s41, v162
	v_mul_f32_e32 v41, s41, v166
	v_mul_f32_e32 v42, s41, v170
	v_mul_f32_e32 v43, s41, v174
	v_med3_f32 v36, v36, s27, v1
	v_med3_f32 v37, v37, s27, v1
	v_med3_f32 v38, v38, s27, v1
	v_med3_f32 v39, v39, s27, v1
	v_med3_f32 v40, v40, s27, v1
	v_med3_f32 v41, v41, s27, v1
	v_med3_f32 v42, v42, s27, v1
	v_med3_f32 v43, v43, s27, v1
	v_cvt_pk_fp8_f32 v32, v36, v37
	v_cvt_pk_fp8_f32 v33, v40, v41
	v_cvt_pk_fp8_f32 v32, v38, v39 op_sel:[0,0,1]
	v_cvt_pk_fp8_f32 v33, v42, v43 op_sel:[0,0,1]
	s_nop 0
	global_store_dwordx2 v23, v[32:33], s[30:31]
	v_mul_f32_e32 v36, s41, v147
	v_mul_f32_e32 v37, s41, v151
	v_mul_f32_e32 v38, s41, v155
	v_mul_f32_e32 v39, s41, v159
	v_mul_f32_e32 v40, s41, v163
	v_mul_f32_e32 v41, s41, v167
	v_mul_f32_e32 v42, s41, v171
	v_mul_f32_e32 v43, s41, v175
	v_med3_f32 v36, v36, s27, v1
	v_med3_f32 v37, v37, s27, v1
	v_med3_f32 v38, v38, s27, v1
	v_med3_f32 v39, v39, s27, v1
	v_med3_f32 v40, v40, s27, v1
	v_med3_f32 v41, v41, s27, v1
	v_med3_f32 v42, v42, s27, v1
	v_med3_f32 v43, v43, s27, v1
	v_cvt_pk_fp8_f32 v34, v36, v37
	v_cvt_pk_fp8_f32 v35, v40, v41
	v_cvt_pk_fp8_f32 v34, v38, v39 op_sel:[0,0,1]
	v_cvt_pk_fp8_f32 v35, v42, v43 op_sel:[0,0,1]
	s_nop 0
	global_store_dwordx2 v24, v[34:35], s[30:31]
	s_branch .Lcv_batch
